# peel+nt plus: back-edge rotation of the 4 GEMM K-loops (loop control + LDS address math before the closing barrier) and LDS-DMA for the up-proj shift-table loads (8 serial round trips removed)
# baseline (speedup 1.0000x reference)
.LBB0_310:
	s_ashr_i32 s91, s90, 31
	s_lshl_b64 s[4:5], s[90:91], 20
	s_add_u32 s62, s66, s4
	s_addc_u32 s63, s67, s5
	s_and_b64 s[4:5], s[36:37], exec
	s_cselect_b32 s4, s63, s25
	s_cselect_b32 s5, s62, s24
	s_ashr_i32 s89, s88, 31
	s_lshl_b64 s[20:21], s[88:89], 20
	s_add_u32 s20, s72, s20
	s_addc_u32 s21, s73, s21
	s_and_b64 s[30:31], s[36:37], exec
	s_cselect_b32 s8, s21, s1
	s_cselect_b32 s13, s20, s0
	s_add_u32 s17, s0, 0x10000
	s_addc_u32 s19, s1, 0
	s_add_u32 s0, s24, 0x80080
	s_addc_u32 s1, s25, 0
	s_mov_b32 s28, -2
	v_add_u32_e32 v100, s3, v190
	v_add_u32_e32 v156, s75, v190
	ds_read_b128 v[40:43], v100
	ds_read_b128 v[60:63], v100 offset:1024
	ds_read_b128 v[80:83], v100 offset:2048
	ds_read_b128 v[100:103], v100 offset:3072
	ds_read_b128 v[120:123], v156
	ds_read_b128 v[140:143], v156 offset:1024
	ds_read_b128 v[152:155], v156 offset:2048
	ds_read_b128 v[156:159], v156 offset:3072
	s_add_u32 s24, s0, 0xfff80080
	s_addc_u32 s25, s1, -1
	s_cmp_eq_u32 s28, 28
	s_cselect_b32 s39, s4, s25
	s_cselect_b32 s38, s5, s24
	s_cselect_b32 s25, s8, s19
	s_cselect_b32 s24, s13, s17
	v_lshl_add_u64 v[188:189], s[0:1], 0, v[168:169]
	s_add_i32 m0, s78, 0xc000
	ds_read_b128 v[172:175], v191
	ds_read_b128 v[176:179], v191 offset:1024
	ds_read_b128 v[180:183], v191 offset:2048
	ds_read_b128 v[184:187], v191 offset:3072
	ds_read_b128 v[192:195], v191 offset:4096
	ds_read_b128 v[196:199], v191 offset:5120
	ds_read_b128 v[200:203], v191 offset:6144
	ds_read_b128 v[204:207], v191 offset:7168
	global_load_lds_dwordx4 v[188:189], off
	v_lshl_add_u64 v[188:189], s[0:1], 0, v[170:171]
	s_add_i32 m0, s78, 0xe000
	s_nop 0
	global_load_lds_dwordx4 v[188:189], off
	s_waitcnt vmcnt(8)
	s_waitcnt lgkmcnt(0)
	s_barrier
	s_setprio 1
	s_waitcnt lgkmcnt(0)
	v_mfma_f32_16x16x32_bf16 v[148:151], v[40:43], v[172:175], 0
	v_mfma_f32_16x16x32_bf16 v[144:147], v[80:83], v[172:175], 0
	v_mfma_f32_16x16x32_bf16 v[128:131], v[40:43], v[180:183], 0
	v_mfma_f32_16x16x32_bf16 v[124:127], v[80:83], v[180:183], 0
	v_mfma_f32_16x16x32_bf16 v[108:111], v[40:43], v[192:195], 0
	v_mfma_f32_16x16x32_bf16 v[104:107], v[80:83], v[192:195], 0
	v_mfma_f32_16x16x32_bf16 v[88:91], v[40:43], v[200:203], 0
	v_mfma_f32_16x16x32_bf16 v[84:87], v[80:83], v[200:203], 0
	v_mfma_f32_16x16x32_bf16 v[148:151], v[60:63], v[176:179], v[148:151]
	v_mfma_f32_16x16x32_bf16 v[144:147], v[100:103], v[176:179], v[144:147]
	v_mfma_f32_16x16x32_bf16 v[128:131], v[60:63], v[184:187], v[128:131]
	v_mfma_f32_16x16x32_bf16 v[124:127], v[100:103], v[184:187], v[124:127]
	v_mfma_f32_16x16x32_bf16 v[108:111], v[60:63], v[196:199], v[108:111]
	v_mfma_f32_16x16x32_bf16 v[104:107], v[100:103], v[196:199], v[104:107]
	v_mfma_f32_16x16x32_bf16 v[88:91], v[60:63], v[204:207], v[88:91]
	v_mfma_f32_16x16x32_bf16 v[84:87], v[100:103], v[204:207], v[84:87]
	s_setprio 0
	s_setprio 1
	v_mfma_f32_16x16x32_bf16 v[136:139], v[120:123], v[172:175], 0
	v_mfma_f32_16x16x32_bf16 v[132:135], v[152:155], v[172:175], 0
	v_mfma_f32_16x16x32_bf16 v[116:119], v[120:123], v[180:183], 0
	v_mfma_f32_16x16x32_bf16 v[112:115], v[152:155], v[180:183], 0
	v_mfma_f32_16x16x32_bf16 v[96:99], v[120:123], v[192:195], 0
	v_mfma_f32_16x16x32_bf16 v[92:95], v[152:155], v[192:195], 0
	v_mfma_f32_16x16x32_bf16 v[76:79], v[120:123], v[200:203], 0
	v_mfma_f32_16x16x32_bf16 v[72:75], v[152:155], v[200:203], 0
	v_mfma_f32_16x16x32_bf16 v[136:139], v[140:143], v[176:179], v[136:139]
	v_mfma_f32_16x16x32_bf16 v[132:135], v[156:159], v[176:179], v[132:135]
	v_mfma_f32_16x16x32_bf16 v[116:119], v[140:143], v[184:187], v[116:119]
	v_mfma_f32_16x16x32_bf16 v[112:115], v[156:159], v[184:187], v[112:115]
	v_mfma_f32_16x16x32_bf16 v[96:99], v[140:143], v[196:199], v[96:99]
	v_mfma_f32_16x16x32_bf16 v[92:95], v[156:159], v[196:199], v[92:95]
	v_mfma_f32_16x16x32_bf16 v[76:79], v[140:143], v[204:207], v[76:79]
	v_mfma_f32_16x16x32_bf16 v[72:75], v[156:159], v[204:207], v[72:75]
	s_setprio 0
	s_barrier
	s_mov_b32 m0, s23
	v_lshl_add_u64 v[188:189], s[24:25], 0, v[162:163]
	s_add_u32 s30, s24, 0x4000
	ds_read_b128 v[172:175], v191 offset:16384
	ds_read_b128 v[176:179], v191 offset:17408
	ds_read_b128 v[180:183], v191 offset:18432
	ds_read_b128 v[184:187], v191 offset:19456
	ds_read_b128 v[192:195], v191 offset:20480
	ds_read_b128 v[196:199], v191 offset:21504
	ds_read_b128 v[200:203], v191 offset:22528
	ds_read_b128 v[204:207], v191 offset:23552
	global_load_lds_dwordx4 v[188:189], off
	v_lshl_add_u64 v[188:189], s[24:25], 0, v[166:167]
	s_mov_b32 m0, s74
	s_addc_u32 s31, s25, 0
	global_load_lds_dwordx4 v[188:189], off
	v_lshl_add_u64 v[188:189], s[30:31], 0, v[162:163]
	s_mov_b32 m0, s76
	v_lshl_add_u64 v[208:209], s[38:39], 0, v[164:165]
	global_load_lds_dwordx4 v[188:189], off
	v_lshl_add_u64 v[188:189], s[30:31], 0, v[166:167]
	s_mov_b32 m0, s77
	s_nop 0
	global_load_lds_dwordx4 v[188:189], off
	v_lshl_add_u64 v[188:189], s[38:39], 0, v[160:161]
	s_mov_b32 m0, s78
	s_nop 0
	global_load_lds_dwordx4 v[188:189], off
	s_mov_b32 m0, s79
	s_nop 0
	global_load_lds_dwordx4 v[208:209], off
	s_waitcnt vmcnt(8)
	s_waitcnt lgkmcnt(0)
	s_barrier
	s_setprio 1
	s_waitcnt lgkmcnt(0)
	v_mfma_f32_16x16x32_bf16 v[68:71], v[40:43], v[172:175], 0
	v_mfma_f32_16x16x32_bf16 v[64:67], v[80:83], v[172:175], 0
	v_mfma_f32_16x16x32_bf16 v[48:51], v[40:43], v[180:183], 0
	v_mfma_f32_16x16x32_bf16 v[44:47], v[80:83], v[180:183], 0
	v_mfma_f32_16x16x32_bf16 v[28:31], v[40:43], v[192:195], 0
	v_mfma_f32_16x16x32_bf16 v[24:27], v[80:83], v[192:195], 0
	v_mfma_f32_16x16x32_bf16 v[12:15], v[40:43], v[200:203], 0
	v_mfma_f32_16x16x32_bf16 v[8:11], v[80:83], v[200:203], 0
	v_mfma_f32_16x16x32_bf16 v[68:71], v[60:63], v[176:179], v[68:71]
	v_mfma_f32_16x16x32_bf16 v[64:67], v[100:103], v[176:179], v[64:67]
	v_mfma_f32_16x16x32_bf16 v[48:51], v[60:63], v[184:187], v[48:51]
	v_mfma_f32_16x16x32_bf16 v[44:47], v[100:103], v[184:187], v[44:47]
	v_mfma_f32_16x16x32_bf16 v[28:31], v[60:63], v[196:199], v[28:31]
	v_mfma_f32_16x16x32_bf16 v[24:27], v[100:103], v[196:199], v[24:27]
	v_mfma_f32_16x16x32_bf16 v[12:15], v[60:63], v[204:207], v[12:15]
	v_mfma_f32_16x16x32_bf16 v[8:11], v[100:103], v[204:207], v[8:11]
	s_setprio 0
	s_setprio 1
	v_mfma_f32_16x16x32_bf16 v[52:55], v[152:155], v[172:175], 0
	v_mfma_f32_16x16x32_bf16 v[36:39], v[120:123], v[180:183], 0
	v_mfma_f32_16x16x32_bf16 v[32:35], v[152:155], v[180:183], 0
	v_mfma_f32_16x16x32_bf16 v[20:23], v[120:123], v[192:195], 0
	v_mfma_f32_16x16x32_bf16 v[16:19], v[152:155], v[192:195], 0
	v_mfma_f32_16x16x32_bf16 v[4:7], v[120:123], v[200:203], 0
	v_mfma_f32_16x16x32_bf16 v[0:3], v[152:155], v[200:203], 0
	v_mfma_f32_16x16x32_bf16 v[40:43], v[120:123], v[172:175], 0
	v_mfma_f32_16x16x32_bf16 v[52:55], v[156:159], v[176:179], v[52:55]
	v_mfma_f32_16x16x32_bf16 v[36:39], v[140:143], v[184:187], v[36:39]
	v_mfma_f32_16x16x32_bf16 v[32:35], v[156:159], v[184:187], v[32:35]
	v_mfma_f32_16x16x32_bf16 v[20:23], v[140:143], v[196:199], v[20:23]
	v_mfma_f32_16x16x32_bf16 v[16:19], v[156:159], v[196:199], v[16:19]
	v_mfma_f32_16x16x32_bf16 v[4:7], v[140:143], v[204:207], v[4:7]
	v_mfma_f32_16x16x32_bf16 v[0:3], v[156:159], v[204:207], v[0:3]
	v_mfma_f32_16x16x32_bf16 v[40:43], v[140:143], v[176:179], v[40:43]
	s_setprio 0
	s_barrier
	v_add_u32_e32 v100, s86, v190
	v_add_u32_e32 v156, s95, v190
	ds_read_b128 v[56:59], v100
	ds_read_b128 v[60:63], v100 offset:1024
	ds_read_b128 v[80:83], v100 offset:2048
	ds_read_b128 v[100:103], v100 offset:3072
	ds_read_b128 v[120:123], v156
	ds_read_b128 v[140:143], v156 offset:1024
	ds_read_b128 v[152:155], v156 offset:2048
	ds_read_b128 v[156:159], v156 offset:3072
	s_add_u32 s30, s38, 0x80000
	s_addc_u32 s31, s39, 0
	s_mov_b32 m0, s82
	v_lshl_add_u64 v[210:211], s[30:31], 0, v[160:161]
	ds_read_b128 v[172:175], v191 offset:32768
	ds_read_b128 v[176:179], v191 offset:33792
	ds_read_b128 v[180:183], v191 offset:34816
	ds_read_b128 v[184:187], v191 offset:35840
	ds_read_b128 v[192:195], v191 offset:36864
	ds_read_b128 v[196:199], v191 offset:37888
	ds_read_b128 v[200:203], v191 offset:38912
	ds_read_b128 v[204:207], v191 offset:39936
	global_load_lds_dwordx4 v[210:211], off
	v_lshl_add_u64 v[210:211], s[30:31], 0, v[164:165]
	s_mov_b32 m0, s83
	s_nop 0
	global_load_lds_dwordx4 v[210:211], off
	s_waitcnt vmcnt(8)
	s_waitcnt lgkmcnt(0)
	s_barrier
	s_setprio 1
	s_waitcnt lgkmcnt(0)
	v_mfma_f32_16x16x32_bf16 v[148:151], v[56:59], v[172:175], v[148:151]
	v_mfma_f32_16x16x32_bf16 v[144:147], v[80:83], v[172:175], v[144:147]
	v_mfma_f32_16x16x32_bf16 v[128:131], v[56:59], v[180:183], v[128:131]
	v_mfma_f32_16x16x32_bf16 v[124:127], v[80:83], v[180:183], v[124:127]
	v_mfma_f32_16x16x32_bf16 v[108:111], v[56:59], v[192:195], v[108:111]
	v_mfma_f32_16x16x32_bf16 v[104:107], v[80:83], v[192:195], v[104:107]
	v_mfma_f32_16x16x32_bf16 v[88:91], v[56:59], v[200:203], v[88:91]
	v_mfma_f32_16x16x32_bf16 v[84:87], v[80:83], v[200:203], v[84:87]
	v_mfma_f32_16x16x32_bf16 v[148:151], v[60:63], v[176:179], v[148:151]
	v_mfma_f32_16x16x32_bf16 v[144:147], v[100:103], v[176:179], v[144:147]
	v_mfma_f32_16x16x32_bf16 v[128:131], v[60:63], v[184:187], v[128:131]
	v_mfma_f32_16x16x32_bf16 v[124:127], v[100:103], v[184:187], v[124:127]
	v_mfma_f32_16x16x32_bf16 v[108:111], v[60:63], v[196:199], v[108:111]
	v_mfma_f32_16x16x32_bf16 v[104:107], v[100:103], v[196:199], v[104:107]
	v_mfma_f32_16x16x32_bf16 v[88:91], v[60:63], v[204:207], v[88:91]
	v_mfma_f32_16x16x32_bf16 v[84:87], v[100:103], v[204:207], v[84:87]
	s_setprio 0
	s_setprio 1
	v_mfma_f32_16x16x32_bf16 v[136:139], v[120:123], v[172:175], v[136:139]
	v_mfma_f32_16x16x32_bf16 v[132:135], v[152:155], v[172:175], v[132:135]
	v_mfma_f32_16x16x32_bf16 v[116:119], v[120:123], v[180:183], v[116:119]
	v_mfma_f32_16x16x32_bf16 v[112:115], v[152:155], v[180:183], v[112:115]
	v_mfma_f32_16x16x32_bf16 v[96:99], v[120:123], v[192:195], v[96:99]
	v_mfma_f32_16x16x32_bf16 v[92:95], v[152:155], v[192:195], v[92:95]
	v_mfma_f32_16x16x32_bf16 v[76:79], v[120:123], v[200:203], v[76:79]
	v_mfma_f32_16x16x32_bf16 v[72:75], v[152:155], v[200:203], v[72:75]
	v_mfma_f32_16x16x32_bf16 v[136:139], v[140:143], v[176:179], v[136:139]
	v_mfma_f32_16x16x32_bf16 v[132:135], v[156:159], v[176:179], v[132:135]
	v_mfma_f32_16x16x32_bf16 v[116:119], v[140:143], v[184:187], v[116:119]
	v_mfma_f32_16x16x32_bf16 v[112:115], v[156:159], v[184:187], v[112:115]
	v_mfma_f32_16x16x32_bf16 v[96:99], v[140:143], v[196:199], v[96:99]
	v_mfma_f32_16x16x32_bf16 v[92:95], v[156:159], v[196:199], v[92:95]
	v_mfma_f32_16x16x32_bf16 v[76:79], v[140:143], v[204:207], v[76:79]
	v_mfma_f32_16x16x32_bf16 v[72:75], v[156:159], v[204:207], v[72:75]
	s_setprio 0
	s_barrier
	s_add_u32 s30, s24, 0x8000
	s_addc_u32 s31, s25, 0
	s_mov_b32 m0, s87
	v_lshl_add_u64 v[210:211], s[30:31], 0, v[162:163]
	s_add_u32 s24, s24, 0xc000
	ds_read_b128 v[172:175], v191 offset:49152
	ds_read_b128 v[176:179], v191 offset:50176
	ds_read_b128 v[180:183], v191 offset:51200
	ds_read_b128 v[184:187], v191 offset:52224
	ds_read_b128 v[192:195], v191 offset:53248
	ds_read_b128 v[196:199], v191 offset:54272
	ds_read_b128 v[200:203], v191 offset:55296
	ds_read_b128 v[204:207], v191 offset:56320
	global_load_lds_dwordx4 v[210:211], off
	v_lshl_add_u64 v[210:211], s[30:31], 0, v[166:167]
	s_mov_b32 m0, s92
	s_addc_u32 s25, s25, 0
	global_load_lds_dwordx4 v[210:211], off
	v_lshl_add_u64 v[210:211], s[24:25], 0, v[162:163]
	s_mov_b32 m0, s96
	v_lshl_add_u64 v[188:189], v[188:189], 0, s[26:27]
	global_load_lds_dwordx4 v[210:211], off
	v_lshl_add_u64 v[210:211], s[24:25], 0, v[166:167]
	s_mov_b32 m0, s97
	s_nop 0
	global_load_lds_dwordx4 v[210:211], off
	s_mov_b32 m0, s93
	s_nop 0
	global_load_lds_dwordx4 v[188:189], off
	v_lshl_add_u64 v[188:189], v[208:209], 0, s[26:27]
	s_mov_b32 m0, s94
	s_nop 0
	global_load_lds_dwordx4 v[188:189], off
	s_waitcnt vmcnt(8)
	s_waitcnt lgkmcnt(0)
	s_barrier
	s_setprio 1
	s_waitcnt lgkmcnt(0)
	v_mfma_f32_16x16x32_bf16 v[68:71], v[56:59], v[172:175], v[68:71]
	v_mfma_f32_16x16x32_bf16 v[64:67], v[80:83], v[172:175], v[64:67]
	v_mfma_f32_16x16x32_bf16 v[48:51], v[56:59], v[180:183], v[48:51]
	v_mfma_f32_16x16x32_bf16 v[44:47], v[80:83], v[180:183], v[44:47]
	v_mfma_f32_16x16x32_bf16 v[28:31], v[56:59], v[192:195], v[28:31]
	v_mfma_f32_16x16x32_bf16 v[24:27], v[80:83], v[192:195], v[24:27]
	v_mfma_f32_16x16x32_bf16 v[12:15], v[56:59], v[200:203], v[12:15]
	v_mfma_f32_16x16x32_bf16 v[8:11], v[80:83], v[200:203], v[8:11]
	v_mfma_f32_16x16x32_bf16 v[68:71], v[60:63], v[176:179], v[68:71]
	v_mfma_f32_16x16x32_bf16 v[64:67], v[100:103], v[176:179], v[64:67]
	v_mfma_f32_16x16x32_bf16 v[48:51], v[60:63], v[184:187], v[48:51]
	v_mfma_f32_16x16x32_bf16 v[44:47], v[100:103], v[184:187], v[44:47]
	v_mfma_f32_16x16x32_bf16 v[28:31], v[60:63], v[196:199], v[28:31]
	v_mfma_f32_16x16x32_bf16 v[24:27], v[100:103], v[196:199], v[24:27]
	v_mfma_f32_16x16x32_bf16 v[12:15], v[60:63], v[204:207], v[12:15]
	v_mfma_f32_16x16x32_bf16 v[8:11], v[100:103], v[204:207], v[8:11]
	s_setprio 0
	s_setprio 1
	v_mfma_f32_16x16x32_bf16 v[40:43], v[120:123], v[172:175], v[40:43]
	v_mfma_f32_16x16x32_bf16 v[56:59], v[140:143], v[176:179], v[40:43]
	v_mfma_f32_16x16x32_bf16 v[40:43], v[152:155], v[172:175], v[52:55]
	v_mfma_f32_16x16x32_bf16 v[36:39], v[120:123], v[180:183], v[36:39]
	v_mfma_f32_16x16x32_bf16 v[32:35], v[152:155], v[180:183], v[32:35]
	v_mfma_f32_16x16x32_bf16 v[20:23], v[120:123], v[192:195], v[20:23]
	v_mfma_f32_16x16x32_bf16 v[16:19], v[152:155], v[192:195], v[16:19]
	v_mfma_f32_16x16x32_bf16 v[4:7], v[120:123], v[200:203], v[4:7]
	v_mfma_f32_16x16x32_bf16 v[0:3], v[152:155], v[200:203], v[0:3]
	v_mfma_f32_16x16x32_bf16 v[52:55], v[156:159], v[176:179], v[40:43]
	v_mfma_f32_16x16x32_bf16 v[36:39], v[140:143], v[184:187], v[36:39]
	v_mfma_f32_16x16x32_bf16 v[32:35], v[156:159], v[184:187], v[32:35]
	v_mfma_f32_16x16x32_bf16 v[20:23], v[140:143], v[196:199], v[20:23]
	v_mfma_f32_16x16x32_bf16 v[16:19], v[156:159], v[196:199], v[16:19]
	v_mfma_f32_16x16x32_bf16 v[4:7], v[140:143], v[204:207], v[4:7]
	v_mfma_f32_16x16x32_bf16 v[0:3], v[156:159], v[204:207], v[0:3]
	s_setprio 0
	v_add_u32_e32 v100, s3, v190
	v_add_u32_e32 v156, s75, v190
	s_add_i32 s28, s28, 2
	s_add_u32 s17, s17, 0x10000
	s_addc_u32 s19, s19, 0
	s_add_u32 s0, s0, 0x100
	s_addc_u32 s1, s1, 0
	s_cmp_gt_u32 s28, 29
	s_barrier
.LBB0_311:
	ds_read_b128 v[40:43], v100
	ds_read_b128 v[60:63], v100 offset:1024
	ds_read_b128 v[80:83], v100 offset:2048
	ds_read_b128 v[100:103], v100 offset:3072
	ds_read_b128 v[120:123], v156
	ds_read_b128 v[140:143], v156 offset:1024
	ds_read_b128 v[152:155], v156 offset:2048
	ds_read_b128 v[156:159], v156 offset:3072
	s_add_u32 s24, s0, 0xfff80080
	s_addc_u32 s25, s1, -1
	s_cmp_eq_u32 s28, 28
	s_cselect_b32 s39, s4, s25
	s_cselect_b32 s38, s5, s24
	s_cselect_b32 s25, s8, s19
	s_cselect_b32 s24, s13, s17
	v_lshl_add_u64 v[188:189], s[0:1], 0, v[168:169]
	s_add_i32 m0, s78, 0xc000
	ds_read_b128 v[172:175], v191
	ds_read_b128 v[176:179], v191 offset:1024
	ds_read_b128 v[180:183], v191 offset:2048
	ds_read_b128 v[184:187], v191 offset:3072
	ds_read_b128 v[192:195], v191 offset:4096
	ds_read_b128 v[196:199], v191 offset:5120
	ds_read_b128 v[200:203], v191 offset:6144
	ds_read_b128 v[204:207], v191 offset:7168
	global_load_lds_dwordx4 v[188:189], off
	v_lshl_add_u64 v[188:189], s[0:1], 0, v[170:171]
	s_add_i32 m0, s78, 0xe000
	s_nop 0
	global_load_lds_dwordx4 v[188:189], off
	s_waitcnt vmcnt(8)
	s_waitcnt lgkmcnt(0)
	s_barrier
	s_setprio 1
	s_waitcnt lgkmcnt(0)
	v_mfma_f32_16x16x32_bf16 v[148:151], v[40:43], v[172:175], v[148:151]
	v_mfma_f32_16x16x32_bf16 v[144:147], v[80:83], v[172:175], v[144:147]
	v_mfma_f32_16x16x32_bf16 v[128:131], v[40:43], v[180:183], v[128:131]
	v_mfma_f32_16x16x32_bf16 v[124:127], v[80:83], v[180:183], v[124:127]
	v_mfma_f32_16x16x32_bf16 v[108:111], v[40:43], v[192:195], v[108:111]
	v_mfma_f32_16x16x32_bf16 v[104:107], v[80:83], v[192:195], v[104:107]
	v_mfma_f32_16x16x32_bf16 v[88:91], v[40:43], v[200:203], v[88:91]
	v_mfma_f32_16x16x32_bf16 v[84:87], v[80:83], v[200:203], v[84:87]
	v_mfma_f32_16x16x32_bf16 v[148:151], v[60:63], v[176:179], v[148:151]
	v_mfma_f32_16x16x32_bf16 v[144:147], v[100:103], v[176:179], v[144:147]
	v_mfma_f32_16x16x32_bf16 v[128:131], v[60:63], v[184:187], v[128:131]
	v_mfma_f32_16x16x32_bf16 v[124:127], v[100:103], v[184:187], v[124:127]
	v_mfma_f32_16x16x32_bf16 v[108:111], v[60:63], v[196:199], v[108:111]
	v_mfma_f32_16x16x32_bf16 v[104:107], v[100:103], v[196:199], v[104:107]
	v_mfma_f32_16x16x32_bf16 v[88:91], v[60:63], v[204:207], v[88:91]
	v_mfma_f32_16x16x32_bf16 v[84:87], v[100:103], v[204:207], v[84:87]
	s_setprio 0
	s_setprio 1
	v_mfma_f32_16x16x32_bf16 v[136:139], v[120:123], v[172:175], v[136:139]
	v_mfma_f32_16x16x32_bf16 v[132:135], v[152:155], v[172:175], v[132:135]
	v_mfma_f32_16x16x32_bf16 v[116:119], v[120:123], v[180:183], v[116:119]
	v_mfma_f32_16x16x32_bf16 v[112:115], v[152:155], v[180:183], v[112:115]
	v_mfma_f32_16x16x32_bf16 v[96:99], v[120:123], v[192:195], v[96:99]
	v_mfma_f32_16x16x32_bf16 v[92:95], v[152:155], v[192:195], v[92:95]
	v_mfma_f32_16x16x32_bf16 v[76:79], v[120:123], v[200:203], v[76:79]
	v_mfma_f32_16x16x32_bf16 v[72:75], v[152:155], v[200:203], v[72:75]
	v_mfma_f32_16x16x32_bf16 v[136:139], v[140:143], v[176:179], v[136:139]
	v_mfma_f32_16x16x32_bf16 v[132:135], v[156:159], v[176:179], v[132:135]
	v_mfma_f32_16x16x32_bf16 v[116:119], v[140:143], v[184:187], v[116:119]
	v_mfma_f32_16x16x32_bf16 v[112:115], v[156:159], v[184:187], v[112:115]
	v_mfma_f32_16x16x32_bf16 v[96:99], v[140:143], v[196:199], v[96:99]
	v_mfma_f32_16x16x32_bf16 v[92:95], v[156:159], v[196:199], v[92:95]
	v_mfma_f32_16x16x32_bf16 v[76:79], v[140:143], v[204:207], v[76:79]
	v_mfma_f32_16x16x32_bf16 v[72:75], v[156:159], v[204:207], v[72:75]
	s_setprio 0
	s_barrier
	s_mov_b32 m0, s23
	v_lshl_add_u64 v[188:189], s[24:25], 0, v[162:163]
	s_add_u32 s30, s24, 0x4000
	ds_read_b128 v[172:175], v191 offset:16384
	ds_read_b128 v[176:179], v191 offset:17408
	ds_read_b128 v[180:183], v191 offset:18432
	ds_read_b128 v[184:187], v191 offset:19456
	ds_read_b128 v[192:195], v191 offset:20480
	ds_read_b128 v[196:199], v191 offset:21504
	ds_read_b128 v[200:203], v191 offset:22528
	ds_read_b128 v[204:207], v191 offset:23552
	global_load_lds_dwordx4 v[188:189], off
	v_lshl_add_u64 v[188:189], s[24:25], 0, v[166:167]
	s_mov_b32 m0, s74
	s_addc_u32 s31, s25, 0
	global_load_lds_dwordx4 v[188:189], off
	v_lshl_add_u64 v[188:189], s[30:31], 0, v[162:163]
	s_mov_b32 m0, s76
	v_lshl_add_u64 v[208:209], s[38:39], 0, v[164:165]
	global_load_lds_dwordx4 v[188:189], off
	v_lshl_add_u64 v[188:189], s[30:31], 0, v[166:167]
	s_mov_b32 m0, s77
	s_nop 0
	global_load_lds_dwordx4 v[188:189], off
	v_lshl_add_u64 v[188:189], s[38:39], 0, v[160:161]
	s_mov_b32 m0, s78
	s_nop 0
	global_load_lds_dwordx4 v[188:189], off
	s_mov_b32 m0, s79
	s_nop 0
	global_load_lds_dwordx4 v[208:209], off
	s_waitcnt vmcnt(8)
	s_waitcnt lgkmcnt(0)
	s_barrier
	s_setprio 1
	s_waitcnt lgkmcnt(0)
	v_mfma_f32_16x16x32_bf16 v[68:71], v[40:43], v[172:175], v[68:71]
	v_mfma_f32_16x16x32_bf16 v[64:67], v[80:83], v[172:175], v[64:67]
	v_mfma_f32_16x16x32_bf16 v[48:51], v[40:43], v[180:183], v[48:51]
	v_mfma_f32_16x16x32_bf16 v[44:47], v[80:83], v[180:183], v[44:47]
	v_mfma_f32_16x16x32_bf16 v[28:31], v[40:43], v[192:195], v[28:31]
	v_mfma_f32_16x16x32_bf16 v[24:27], v[80:83], v[192:195], v[24:27]
	v_mfma_f32_16x16x32_bf16 v[12:15], v[40:43], v[200:203], v[12:15]
	v_mfma_f32_16x16x32_bf16 v[8:11], v[80:83], v[200:203], v[8:11]
	v_mfma_f32_16x16x32_bf16 v[68:71], v[60:63], v[176:179], v[68:71]
	v_mfma_f32_16x16x32_bf16 v[64:67], v[100:103], v[176:179], v[64:67]
	v_mfma_f32_16x16x32_bf16 v[48:51], v[60:63], v[184:187], v[48:51]
	v_mfma_f32_16x16x32_bf16 v[44:47], v[100:103], v[184:187], v[44:47]
	v_mfma_f32_16x16x32_bf16 v[28:31], v[60:63], v[196:199], v[28:31]
	v_mfma_f32_16x16x32_bf16 v[24:27], v[100:103], v[196:199], v[24:27]
	v_mfma_f32_16x16x32_bf16 v[12:15], v[60:63], v[204:207], v[12:15]
	v_mfma_f32_16x16x32_bf16 v[8:11], v[100:103], v[204:207], v[8:11]
	s_setprio 0
	s_setprio 1
	v_mfma_f32_16x16x32_bf16 v[52:55], v[152:155], v[172:175], v[52:55]
	v_mfma_f32_16x16x32_bf16 v[36:39], v[120:123], v[180:183], v[36:39]
	v_mfma_f32_16x16x32_bf16 v[32:35], v[152:155], v[180:183], v[32:35]
	v_mfma_f32_16x16x32_bf16 v[20:23], v[120:123], v[192:195], v[20:23]
	v_mfma_f32_16x16x32_bf16 v[16:19], v[152:155], v[192:195], v[16:19]
	v_mfma_f32_16x16x32_bf16 v[4:7], v[120:123], v[200:203], v[4:7]
	v_mfma_f32_16x16x32_bf16 v[0:3], v[152:155], v[200:203], v[0:3]
	v_mfma_f32_16x16x32_bf16 v[40:43], v[120:123], v[172:175], v[56:59]
	v_mfma_f32_16x16x32_bf16 v[52:55], v[156:159], v[176:179], v[52:55]
	v_mfma_f32_16x16x32_bf16 v[36:39], v[140:143], v[184:187], v[36:39]
	v_mfma_f32_16x16x32_bf16 v[32:35], v[156:159], v[184:187], v[32:35]
	v_mfma_f32_16x16x32_bf16 v[20:23], v[140:143], v[196:199], v[20:23]
	v_mfma_f32_16x16x32_bf16 v[16:19], v[156:159], v[196:199], v[16:19]
	v_mfma_f32_16x16x32_bf16 v[4:7], v[140:143], v[204:207], v[4:7]
	v_mfma_f32_16x16x32_bf16 v[0:3], v[156:159], v[204:207], v[0:3]
	v_mfma_f32_16x16x32_bf16 v[40:43], v[140:143], v[176:179], v[40:43]
	s_setprio 0
	s_barrier
	v_add_u32_e32 v100, s86, v190
	v_add_u32_e32 v156, s95, v190
	ds_read_b128 v[56:59], v100
	ds_read_b128 v[60:63], v100 offset:1024
	ds_read_b128 v[80:83], v100 offset:2048
	ds_read_b128 v[100:103], v100 offset:3072
	ds_read_b128 v[120:123], v156
	ds_read_b128 v[140:143], v156 offset:1024
	ds_read_b128 v[152:155], v156 offset:2048
	ds_read_b128 v[156:159], v156 offset:3072
	s_add_u32 s30, s38, 0x80000
	s_addc_u32 s31, s39, 0
	s_mov_b32 m0, s82
	v_lshl_add_u64 v[210:211], s[30:31], 0, v[160:161]
	ds_read_b128 v[172:175], v191 offset:32768
	ds_read_b128 v[176:179], v191 offset:33792
	ds_read_b128 v[180:183], v191 offset:34816
	ds_read_b128 v[184:187], v191 offset:35840
	ds_read_b128 v[192:195], v191 offset:36864
	ds_read_b128 v[196:199], v191 offset:37888
	ds_read_b128 v[200:203], v191 offset:38912
	ds_read_b128 v[204:207], v191 offset:39936
	global_load_lds_dwordx4 v[210:211], off
	v_lshl_add_u64 v[210:211], s[30:31], 0, v[164:165]
	s_mov_b32 m0, s83
	s_nop 0
	global_load_lds_dwordx4 v[210:211], off
	s_waitcnt vmcnt(8)
	s_waitcnt lgkmcnt(0)
	s_barrier
	s_setprio 1
	s_waitcnt lgkmcnt(0)
	v_mfma_f32_16x16x32_bf16 v[148:151], v[56:59], v[172:175], v[148:151]
	v_mfma_f32_16x16x32_bf16 v[144:147], v[80:83], v[172:175], v[144:147]
	v_mfma_f32_16x16x32_bf16 v[128:131], v[56:59], v[180:183], v[128:131]
	v_mfma_f32_16x16x32_bf16 v[124:127], v[80:83], v[180:183], v[124:127]
	v_mfma_f32_16x16x32_bf16 v[108:111], v[56:59], v[192:195], v[108:111]
	v_mfma_f32_16x16x32_bf16 v[104:107], v[80:83], v[192:195], v[104:107]
	v_mfma_f32_16x16x32_bf16 v[88:91], v[56:59], v[200:203], v[88:91]
	v_mfma_f32_16x16x32_bf16 v[84:87], v[80:83], v[200:203], v[84:87]
	v_mfma_f32_16x16x32_bf16 v[148:151], v[60:63], v[176:179], v[148:151]
	v_mfma_f32_16x16x32_bf16 v[144:147], v[100:103], v[176:179], v[144:147]
	v_mfma_f32_16x16x32_bf16 v[128:131], v[60:63], v[184:187], v[128:131]
	v_mfma_f32_16x16x32_bf16 v[124:127], v[100:103], v[184:187], v[124:127]
	v_mfma_f32_16x16x32_bf16 v[108:111], v[60:63], v[196:199], v[108:111]
	v_mfma_f32_16x16x32_bf16 v[104:107], v[100:103], v[196:199], v[104:107]
	v_mfma_f32_16x16x32_bf16 v[88:91], v[60:63], v[204:207], v[88:91]
	v_mfma_f32_16x16x32_bf16 v[84:87], v[100:103], v[204:207], v[84:87]
	s_setprio 0
	s_setprio 1
	v_mfma_f32_16x16x32_bf16 v[136:139], v[120:123], v[172:175], v[136:139]
	v_mfma_f32_16x16x32_bf16 v[132:135], v[152:155], v[172:175], v[132:135]
	v_mfma_f32_16x16x32_bf16 v[116:119], v[120:123], v[180:183], v[116:119]
	v_mfma_f32_16x16x32_bf16 v[112:115], v[152:155], v[180:183], v[112:115]
	v_mfma_f32_16x16x32_bf16 v[96:99], v[120:123], v[192:195], v[96:99]
	v_mfma_f32_16x16x32_bf16 v[92:95], v[152:155], v[192:195], v[92:95]
	v_mfma_f32_16x16x32_bf16 v[76:79], v[120:123], v[200:203], v[76:79]
	v_mfma_f32_16x16x32_bf16 v[72:75], v[152:155], v[200:203], v[72:75]
	v_mfma_f32_16x16x32_bf16 v[136:139], v[140:143], v[176:179], v[136:139]
	v_mfma_f32_16x16x32_bf16 v[132:135], v[156:159], v[176:179], v[132:135]
	v_mfma_f32_16x16x32_bf16 v[116:119], v[140:143], v[184:187], v[116:119]
	v_mfma_f32_16x16x32_bf16 v[112:115], v[156:159], v[184:187], v[112:115]
	v_mfma_f32_16x16x32_bf16 v[96:99], v[140:143], v[196:199], v[96:99]
	v_mfma_f32_16x16x32_bf16 v[92:95], v[156:159], v[196:199], v[92:95]
	v_mfma_f32_16x16x32_bf16 v[76:79], v[140:143], v[204:207], v[76:79]
	v_mfma_f32_16x16x32_bf16 v[72:75], v[156:159], v[204:207], v[72:75]
	s_setprio 0
	s_barrier
	s_add_u32 s30, s24, 0x8000
	s_addc_u32 s31, s25, 0
	s_mov_b32 m0, s87
	v_lshl_add_u64 v[210:211], s[30:31], 0, v[162:163]
	s_add_u32 s24, s24, 0xc000
	ds_read_b128 v[172:175], v191 offset:49152
	ds_read_b128 v[176:179], v191 offset:50176
	ds_read_b128 v[180:183], v191 offset:51200
	ds_read_b128 v[184:187], v191 offset:52224
	ds_read_b128 v[192:195], v191 offset:53248
	ds_read_b128 v[196:199], v191 offset:54272
	ds_read_b128 v[200:203], v191 offset:55296
	ds_read_b128 v[204:207], v191 offset:56320
	global_load_lds_dwordx4 v[210:211], off
	v_lshl_add_u64 v[210:211], s[30:31], 0, v[166:167]
	s_mov_b32 m0, s92
	s_addc_u32 s25, s25, 0
	global_load_lds_dwordx4 v[210:211], off
	v_lshl_add_u64 v[210:211], s[24:25], 0, v[162:163]
	s_mov_b32 m0, s96
	v_lshl_add_u64 v[188:189], v[188:189], 0, s[26:27]
	global_load_lds_dwordx4 v[210:211], off
	v_lshl_add_u64 v[210:211], s[24:25], 0, v[166:167]
	s_mov_b32 m0, s97
	s_nop 0
	global_load_lds_dwordx4 v[210:211], off
	s_mov_b32 m0, s93
	s_nop 0
	global_load_lds_dwordx4 v[188:189], off
	v_lshl_add_u64 v[188:189], v[208:209], 0, s[26:27]
	s_mov_b32 m0, s94
	s_nop 0
	global_load_lds_dwordx4 v[188:189], off
	s_waitcnt vmcnt(8)
	s_waitcnt lgkmcnt(0)
	s_barrier
	s_setprio 1
	s_waitcnt lgkmcnt(0)
	v_mfma_f32_16x16x32_bf16 v[68:71], v[56:59], v[172:175], v[68:71]
	v_mfma_f32_16x16x32_bf16 v[64:67], v[80:83], v[172:175], v[64:67]
	v_mfma_f32_16x16x32_bf16 v[48:51], v[56:59], v[180:183], v[48:51]
	v_mfma_f32_16x16x32_bf16 v[44:47], v[80:83], v[180:183], v[44:47]
	v_mfma_f32_16x16x32_bf16 v[28:31], v[56:59], v[192:195], v[28:31]
	v_mfma_f32_16x16x32_bf16 v[24:27], v[80:83], v[192:195], v[24:27]
	v_mfma_f32_16x16x32_bf16 v[12:15], v[56:59], v[200:203], v[12:15]
	v_mfma_f32_16x16x32_bf16 v[8:11], v[80:83], v[200:203], v[8:11]
	v_mfma_f32_16x16x32_bf16 v[68:71], v[60:63], v[176:179], v[68:71]
	v_mfma_f32_16x16x32_bf16 v[64:67], v[100:103], v[176:179], v[64:67]
	v_mfma_f32_16x16x32_bf16 v[48:51], v[60:63], v[184:187], v[48:51]
	v_mfma_f32_16x16x32_bf16 v[44:47], v[100:103], v[184:187], v[44:47]
	v_mfma_f32_16x16x32_bf16 v[28:31], v[60:63], v[196:199], v[28:31]
	v_mfma_f32_16x16x32_bf16 v[24:27], v[100:103], v[196:199], v[24:27]
	v_mfma_f32_16x16x32_bf16 v[12:15], v[60:63], v[204:207], v[12:15]
	v_mfma_f32_16x16x32_bf16 v[8:11], v[100:103], v[204:207], v[8:11]
	s_setprio 0
	s_setprio 1
	v_mfma_f32_16x16x32_bf16 v[40:43], v[120:123], v[172:175], v[40:43]
	v_mfma_f32_16x16x32_bf16 v[56:59], v[140:143], v[176:179], v[40:43]
	v_mfma_f32_16x16x32_bf16 v[40:43], v[152:155], v[172:175], v[52:55]
	v_mfma_f32_16x16x32_bf16 v[36:39], v[120:123], v[180:183], v[36:39]
	v_mfma_f32_16x16x32_bf16 v[32:35], v[152:155], v[180:183], v[32:35]
	v_mfma_f32_16x16x32_bf16 v[20:23], v[120:123], v[192:195], v[20:23]
	v_mfma_f32_16x16x32_bf16 v[16:19], v[152:155], v[192:195], v[16:19]
	v_mfma_f32_16x16x32_bf16 v[4:7], v[120:123], v[200:203], v[4:7]
	v_mfma_f32_16x16x32_bf16 v[0:3], v[152:155], v[200:203], v[0:3]
	v_mfma_f32_16x16x32_bf16 v[52:55], v[156:159], v[176:179], v[40:43]
	v_mfma_f32_16x16x32_bf16 v[36:39], v[140:143], v[184:187], v[36:39]
	v_mfma_f32_16x16x32_bf16 v[32:35], v[156:159], v[184:187], v[32:35]
	v_mfma_f32_16x16x32_bf16 v[20:23], v[140:143], v[196:199], v[20:23]
	v_mfma_f32_16x16x32_bf16 v[16:19], v[156:159], v[196:199], v[16:19]
	v_mfma_f32_16x16x32_bf16 v[4:7], v[140:143], v[204:207], v[4:7]
	v_mfma_f32_16x16x32_bf16 v[0:3], v[156:159], v[204:207], v[0:3]
	s_setprio 0
	v_add_u32_e32 v100, s3, v190
	v_add_u32_e32 v156, s75, v190
	s_add_i32 s28, s28, 2
	s_add_u32 s17, s17, 0x10000
	s_addc_u32 s19, s19, 0
	s_add_u32 s0, s0, 0x100
	s_addc_u32 s1, s1, 0
	s_cmp_gt_u32 s28, 29
	s_barrier
	s_cbranch_scc0 .LBB0_311
	s_and_b64 vcc, exec, s[34:35]
	s_cbranch_vccz .LBB0_314
	s_barrier

.LBB0_1054:
	s_ashr_i32 s41, s40, 31
	s_lshl_b64 s[4:5], s[40:41], 20
	s_add_u32 s44, s16, s4
	s_addc_u32 s45, s17, s5
	s_and_b64 s[4:5], s[36:37], exec
	s_cselect_b32 s4, s45, s51
	s_cselect_b32 s5, s44, s50
	s_ashr_i32 s39, s38, 31
	s_lshl_b64 s[46:47], s[38:39], 20
	s_add_u32 s46, s18, s46
	s_addc_u32 s47, s19, s47
	s_and_b64 s[52:53], s[36:37], exec
	s_cselect_b32 s39, s47, s1
	s_cselect_b32 s41, s46, s0
	s_add_u32 s49, s0, 0x10000
	s_addc_u32 s55, s1, 0
	s_add_u32 s0, s50, 0x80080
	s_addc_u32 s1, s51, 0
	s_mov_b32 s80, -2
	v_add_u32_e32 v140, s28, v215
	v_add_u32_e32 v156, s54, v215
	ds_read_b128 v[128:131], v140
	ds_read_b128 v[132:135], v140 offset:1024
	ds_read_b128 v[136:139], v140 offset:2048
	ds_read_b128 v[140:143], v140 offset:3072
	ds_read_b128 v[144:147], v156
	ds_read_b128 v[148:151], v156 offset:1024
	ds_read_b128 v[152:155], v156 offset:2048
	ds_read_b128 v[156:159], v156 offset:3072
	s_add_u32 s50, s0, 0xfff80080
	s_addc_u32 s51, s1, -1
	s_cmp_eq_u32 s80, 28
	s_cselect_b32 s53, s4, s51
	s_cselect_b32 s52, s5, s50
	s_cselect_b32 s51, s39, s55
	s_cselect_b32 s50, s41, s49
	v_lshl_add_u64 v[204:205], s[0:1], 0, v[180:181]
	s_add_i32 m0, s58, 0xc000
	ds_read_b128 v[160:163], v251
	ds_read_b128 v[164:167], v251 offset:1024
	ds_read_b128 v[168:171], v251 offset:2048
	ds_read_b128 v[184:187], v251 offset:3072
	ds_read_b128 v[188:191], v251 offset:4096
	ds_read_b128 v[192:195], v251 offset:5120
	ds_read_b128 v[196:199], v251 offset:6144
	ds_read_b128 v[200:203], v251 offset:7168
	global_load_lds_dwordx4 v[204:205], off
	v_lshl_add_u64 v[204:205], s[0:1], 0, v[182:183]
	s_add_i32 m0, s58, 0xe000
	s_nop 0
	global_load_lds_dwordx4 v[204:205], off
	s_waitcnt vmcnt(8)
	s_waitcnt lgkmcnt(0)
	s_barrier
	s_setprio 1
	s_waitcnt lgkmcnt(0)
	v_mfma_f32_16x16x32_bf16 v[124:127], v[128:131], v[160:163], 0
	v_mfma_f32_16x16x32_bf16 v[120:123], v[136:139], v[160:163], 0
	v_mfma_f32_16x16x32_bf16 v[116:119], v[128:131], v[168:171], 0
	v_mfma_f32_16x16x32_bf16 v[112:115], v[136:139], v[168:171], 0
	v_mfma_f32_16x16x32_bf16 v[108:111], v[128:131], v[188:191], 0
	v_mfma_f32_16x16x32_bf16 v[104:107], v[136:139], v[188:191], 0
	v_mfma_f32_16x16x32_bf16 v[100:103], v[128:131], v[196:199], 0
	v_mfma_f32_16x16x32_bf16 v[96:99], v[136:139], v[196:199], 0
	v_mfma_f32_16x16x32_bf16 v[124:127], v[132:135], v[164:167], v[124:127]
	v_mfma_f32_16x16x32_bf16 v[120:123], v[140:143], v[164:167], v[120:123]
	v_mfma_f32_16x16x32_bf16 v[116:119], v[132:135], v[184:187], v[116:119]
	v_mfma_f32_16x16x32_bf16 v[112:115], v[140:143], v[184:187], v[112:115]
	v_mfma_f32_16x16x32_bf16 v[108:111], v[132:135], v[192:195], v[108:111]
	v_mfma_f32_16x16x32_bf16 v[104:107], v[140:143], v[192:195], v[104:107]
	v_mfma_f32_16x16x32_bf16 v[100:103], v[132:135], v[200:203], v[100:103]
	v_mfma_f32_16x16x32_bf16 v[96:99], v[140:143], v[200:203], v[96:99]
	s_setprio 0
	s_setprio 1
	v_mfma_f32_16x16x32_bf16 v[60:63], v[144:147], v[160:163], 0
	v_mfma_f32_16x16x32_bf16 v[56:59], v[152:155], v[160:163], 0
	v_mfma_f32_16x16x32_bf16 v[52:55], v[144:147], v[168:171], 0
	v_mfma_f32_16x16x32_bf16 v[48:51], v[152:155], v[168:171], 0
	v_mfma_f32_16x16x32_bf16 v[44:47], v[144:147], v[188:191], 0
	v_mfma_f32_16x16x32_bf16 v[40:43], v[152:155], v[188:191], 0
	v_mfma_f32_16x16x32_bf16 v[36:39], v[144:147], v[196:199], 0
	v_mfma_f32_16x16x32_bf16 v[32:35], v[152:155], v[196:199], 0
	v_mfma_f32_16x16x32_bf16 v[60:63], v[148:151], v[164:167], v[60:63]
	v_mfma_f32_16x16x32_bf16 v[56:59], v[156:159], v[164:167], v[56:59]
	v_mfma_f32_16x16x32_bf16 v[52:55], v[148:151], v[184:187], v[52:55]
	v_mfma_f32_16x16x32_bf16 v[48:51], v[156:159], v[184:187], v[48:51]
	v_mfma_f32_16x16x32_bf16 v[44:47], v[148:151], v[192:195], v[44:47]
	v_mfma_f32_16x16x32_bf16 v[40:43], v[156:159], v[192:195], v[40:43]
	v_mfma_f32_16x16x32_bf16 v[36:39], v[148:151], v[200:203], v[36:39]
	v_mfma_f32_16x16x32_bf16 v[32:35], v[156:159], v[200:203], v[32:35]
	s_setprio 0
	s_barrier
	s_mov_b32 m0, s30
	v_lshl_add_u64 v[204:205], s[50:51], 0, v[174:175]
	s_add_u32 s82, s50, 0x4000
	ds_read_b128 v[160:163], v251 offset:16384
	ds_read_b128 v[164:167], v251 offset:17408
	ds_read_b128 v[168:171], v251 offset:18432
	ds_read_b128 v[184:187], v251 offset:19456
	ds_read_b128 v[188:191], v251 offset:20480
	ds_read_b128 v[192:195], v251 offset:21504
	ds_read_b128 v[196:199], v251 offset:22528
	ds_read_b128 v[200:203], v251 offset:23552
	global_load_lds_dwordx4 v[204:205], off
	v_lshl_add_u64 v[204:205], s[50:51], 0, v[178:179]
	s_mov_b32 m0, s43
	s_addc_u32 s83, s51, 0
	global_load_lds_dwordx4 v[204:205], off
	v_lshl_add_u64 v[204:205], s[82:83], 0, v[174:175]
	s_mov_b32 m0, s56
	v_lshl_add_u64 v[206:207], s[52:53], 0, v[176:177]
	global_load_lds_dwordx4 v[204:205], off
	v_lshl_add_u64 v[204:205], s[82:83], 0, v[178:179]
	s_mov_b32 m0, s57
	s_nop 0
	global_load_lds_dwordx4 v[204:205], off
	v_lshl_add_u64 v[204:205], s[52:53], 0, v[172:173]
	s_mov_b32 m0, s58
	s_nop 0
	global_load_lds_dwordx4 v[204:205], off
	s_mov_b32 m0, s59
	s_nop 0
	global_load_lds_dwordx4 v[206:207], off
	s_waitcnt vmcnt(8)
	s_waitcnt lgkmcnt(0)
	s_barrier
	s_setprio 1
	s_waitcnt lgkmcnt(0)
	v_mfma_f32_16x16x32_bf16 v[92:95], v[128:131], v[160:163], 0
	v_mfma_f32_16x16x32_bf16 v[88:91], v[136:139], v[160:163], 0
	v_mfma_f32_16x16x32_bf16 v[84:87], v[128:131], v[168:171], 0
	v_mfma_f32_16x16x32_bf16 v[80:83], v[136:139], v[168:171], 0
	v_mfma_f32_16x16x32_bf16 v[76:79], v[128:131], v[188:191], 0
	v_mfma_f32_16x16x32_bf16 v[72:75], v[136:139], v[188:191], 0
	v_mfma_f32_16x16x32_bf16 v[68:71], v[128:131], v[196:199], 0
	v_mfma_f32_16x16x32_bf16 v[64:67], v[136:139], v[196:199], 0
	v_mfma_f32_16x16x32_bf16 v[92:95], v[132:135], v[164:167], v[92:95]
	v_mfma_f32_16x16x32_bf16 v[88:91], v[140:143], v[164:167], v[88:91]
	v_mfma_f32_16x16x32_bf16 v[84:87], v[132:135], v[184:187], v[84:87]
	v_mfma_f32_16x16x32_bf16 v[80:83], v[140:143], v[184:187], v[80:83]
	v_mfma_f32_16x16x32_bf16 v[76:79], v[132:135], v[192:195], v[76:79]
	v_mfma_f32_16x16x32_bf16 v[72:75], v[140:143], v[192:195], v[72:75]
	v_mfma_f32_16x16x32_bf16 v[68:71], v[132:135], v[200:203], v[68:71]
	v_mfma_f32_16x16x32_bf16 v[64:67], v[140:143], v[200:203], v[64:67]
	s_setprio 0
	s_setprio 1
	v_mfma_f32_16x16x32_bf16 v[28:31], v[144:147], v[160:163], 0
	v_mfma_f32_16x16x32_bf16 v[24:27], v[152:155], v[160:163], 0
	v_mfma_f32_16x16x32_bf16 v[20:23], v[144:147], v[168:171], 0
	v_mfma_f32_16x16x32_bf16 v[16:19], v[152:155], v[168:171], 0
	v_mfma_f32_16x16x32_bf16 v[12:15], v[144:147], v[188:191], 0
	v_mfma_f32_16x16x32_bf16 v[8:11], v[152:155], v[188:191], 0
	v_mfma_f32_16x16x32_bf16 v[4:7], v[144:147], v[196:199], 0
	v_mfma_f32_16x16x32_bf16 v[0:3], v[152:155], v[196:199], 0
	v_mfma_f32_16x16x32_bf16 v[28:31], v[148:151], v[164:167], v[28:31]
	v_mfma_f32_16x16x32_bf16 v[24:27], v[156:159], v[164:167], v[24:27]
	v_mfma_f32_16x16x32_bf16 v[20:23], v[148:151], v[184:187], v[20:23]
	v_mfma_f32_16x16x32_bf16 v[16:19], v[156:159], v[184:187], v[16:19]
	v_mfma_f32_16x16x32_bf16 v[12:15], v[148:151], v[192:195], v[12:15]
	v_mfma_f32_16x16x32_bf16 v[8:11], v[156:159], v[192:195], v[8:11]
	v_mfma_f32_16x16x32_bf16 v[4:7], v[148:151], v[200:203], v[4:7]
	v_mfma_f32_16x16x32_bf16 v[0:3], v[156:159], v[200:203], v[0:3]
	s_setprio 0
	s_barrier
	v_add_u32_e32 v140, s68, v215
	v_add_u32_e32 v156, s73, v215
	ds_read_b128 v[128:131], v140
	ds_read_b128 v[132:135], v140 offset:1024
	ds_read_b128 v[136:139], v140 offset:2048
	ds_read_b128 v[140:143], v140 offset:3072
	ds_read_b128 v[144:147], v156
	ds_read_b128 v[148:151], v156 offset:1024
	ds_read_b128 v[152:155], v156 offset:2048
	ds_read_b128 v[156:159], v156 offset:3072
	s_add_u32 s52, s52, 0x80000
	s_addc_u32 s53, s53, 0
	s_mov_b32 m0, s60
	v_lshl_add_u64 v[208:209], s[52:53], 0, v[172:173]
	ds_read_b128 v[160:163], v251 offset:32768
	ds_read_b128 v[164:167], v251 offset:33792
	ds_read_b128 v[168:171], v251 offset:34816
	ds_read_b128 v[184:187], v251 offset:35840
	ds_read_b128 v[188:191], v251 offset:36864
	ds_read_b128 v[192:195], v251 offset:37888
	ds_read_b128 v[196:199], v251 offset:38912
	ds_read_b128 v[200:203], v251 offset:39936
	global_load_lds_dwordx4 v[208:209], off
	v_lshl_add_u64 v[208:209], s[52:53], 0, v[176:177]
	s_mov_b32 m0, s61
	s_nop 0
	global_load_lds_dwordx4 v[208:209], off
	s_waitcnt vmcnt(8)
	s_waitcnt lgkmcnt(0)
	s_barrier
	s_setprio 1
	s_waitcnt lgkmcnt(0)
	v_mfma_f32_16x16x32_bf16 v[124:127], v[128:131], v[160:163], v[124:127]
	v_mfma_f32_16x16x32_bf16 v[120:123], v[136:139], v[160:163], v[120:123]
	v_mfma_f32_16x16x32_bf16 v[116:119], v[128:131], v[168:171], v[116:119]
	v_mfma_f32_16x16x32_bf16 v[112:115], v[136:139], v[168:171], v[112:115]
	v_mfma_f32_16x16x32_bf16 v[108:111], v[128:131], v[188:191], v[108:111]
	v_mfma_f32_16x16x32_bf16 v[104:107], v[136:139], v[188:191], v[104:107]
	v_mfma_f32_16x16x32_bf16 v[100:103], v[128:131], v[196:199], v[100:103]
	v_mfma_f32_16x16x32_bf16 v[96:99], v[136:139], v[196:199], v[96:99]
	v_mfma_f32_16x16x32_bf16 v[124:127], v[132:135], v[164:167], v[124:127]
	v_mfma_f32_16x16x32_bf16 v[120:123], v[140:143], v[164:167], v[120:123]
	v_mfma_f32_16x16x32_bf16 v[116:119], v[132:135], v[184:187], v[116:119]
	v_mfma_f32_16x16x32_bf16 v[112:115], v[140:143], v[184:187], v[112:115]
	v_mfma_f32_16x16x32_bf16 v[108:111], v[132:135], v[192:195], v[108:111]
	v_mfma_f32_16x16x32_bf16 v[104:107], v[140:143], v[192:195], v[104:107]
	v_mfma_f32_16x16x32_bf16 v[100:103], v[132:135], v[200:203], v[100:103]
	v_mfma_f32_16x16x32_bf16 v[96:99], v[140:143], v[200:203], v[96:99]
	s_setprio 0
	s_setprio 1
	v_mfma_f32_16x16x32_bf16 v[60:63], v[144:147], v[160:163], v[60:63]
	v_mfma_f32_16x16x32_bf16 v[56:59], v[152:155], v[160:163], v[56:59]
	v_mfma_f32_16x16x32_bf16 v[52:55], v[144:147], v[168:171], v[52:55]
	v_mfma_f32_16x16x32_bf16 v[48:51], v[152:155], v[168:171], v[48:51]
	v_mfma_f32_16x16x32_bf16 v[44:47], v[144:147], v[188:191], v[44:47]
	v_mfma_f32_16x16x32_bf16 v[40:43], v[152:155], v[188:191], v[40:43]
	v_mfma_f32_16x16x32_bf16 v[36:39], v[144:147], v[196:199], v[36:39]
	v_mfma_f32_16x16x32_bf16 v[32:35], v[152:155], v[196:199], v[32:35]
	v_mfma_f32_16x16x32_bf16 v[60:63], v[148:151], v[164:167], v[60:63]
	v_mfma_f32_16x16x32_bf16 v[56:59], v[156:159], v[164:167], v[56:59]
	v_mfma_f32_16x16x32_bf16 v[52:55], v[148:151], v[184:187], v[52:55]
	v_mfma_f32_16x16x32_bf16 v[48:51], v[156:159], v[184:187], v[48:51]
	v_mfma_f32_16x16x32_bf16 v[44:47], v[148:151], v[192:195], v[44:47]
	v_mfma_f32_16x16x32_bf16 v[40:43], v[156:159], v[192:195], v[40:43]
	v_mfma_f32_16x16x32_bf16 v[36:39], v[148:151], v[200:203], v[36:39]
	v_mfma_f32_16x16x32_bf16 v[32:35], v[156:159], v[200:203], v[32:35]
	s_setprio 0
	s_barrier
	s_add_u32 s52, s50, 0x8000
	s_addc_u32 s53, s51, 0
	s_mov_b32 m0, s69
	v_lshl_add_u64 v[208:209], s[52:53], 0, v[174:175]
	s_add_u32 s50, s50, 0xc000
	ds_read_b128 v[160:163], v251 offset:49152
	ds_read_b128 v[164:167], v251 offset:50176
	ds_read_b128 v[168:171], v251 offset:51200
	ds_read_b128 v[184:187], v251 offset:52224
	ds_read_b128 v[188:191], v251 offset:53248
	ds_read_b128 v[192:195], v251 offset:54272
	ds_read_b128 v[196:199], v251 offset:55296
	ds_read_b128 v[200:203], v251 offset:56320
	global_load_lds_dwordx4 v[208:209], off
	v_lshl_add_u64 v[208:209], s[52:53], 0, v[178:179]
	s_mov_b32 m0, s70
	s_addc_u32 s51, s51, 0
	global_load_lds_dwordx4 v[208:209], off
	v_lshl_add_u64 v[208:209], s[50:51], 0, v[174:175]
	s_mov_b32 m0, s74
	v_lshl_add_u64 v[204:205], v[204:205], 0, s[26:27]
	global_load_lds_dwordx4 v[208:209], off
	v_lshl_add_u64 v[208:209], s[50:51], 0, v[178:179]
	s_mov_b32 m0, s75
	s_nop 0
	global_load_lds_dwordx4 v[208:209], off
	s_mov_b32 m0, s71
	s_nop 0
	global_load_lds_dwordx4 v[204:205], off
	v_lshl_add_u64 v[204:205], v[206:207], 0, s[26:27]
	s_mov_b32 m0, s72
	s_nop 0
	global_load_lds_dwordx4 v[204:205], off
	s_waitcnt vmcnt(8)
	s_waitcnt lgkmcnt(0)
	s_barrier
	s_setprio 1
	s_waitcnt lgkmcnt(0)
	v_mfma_f32_16x16x32_bf16 v[92:95], v[128:131], v[160:163], v[92:95]
	v_mfma_f32_16x16x32_bf16 v[88:91], v[136:139], v[160:163], v[88:91]
	v_mfma_f32_16x16x32_bf16 v[84:87], v[128:131], v[168:171], v[84:87]
	v_mfma_f32_16x16x32_bf16 v[80:83], v[136:139], v[168:171], v[80:83]
	v_mfma_f32_16x16x32_bf16 v[76:79], v[128:131], v[188:191], v[76:79]
	v_mfma_f32_16x16x32_bf16 v[72:75], v[136:139], v[188:191], v[72:75]
	v_mfma_f32_16x16x32_bf16 v[68:71], v[128:131], v[196:199], v[68:71]
	v_mfma_f32_16x16x32_bf16 v[64:67], v[136:139], v[196:199], v[64:67]
	v_mfma_f32_16x16x32_bf16 v[92:95], v[132:135], v[164:167], v[92:95]
	v_mfma_f32_16x16x32_bf16 v[88:91], v[140:143], v[164:167], v[88:91]
	v_mfma_f32_16x16x32_bf16 v[84:87], v[132:135], v[184:187], v[84:87]
	v_mfma_f32_16x16x32_bf16 v[80:83], v[140:143], v[184:187], v[80:83]
	v_mfma_f32_16x16x32_bf16 v[76:79], v[132:135], v[192:195], v[76:79]
	v_mfma_f32_16x16x32_bf16 v[72:75], v[140:143], v[192:195], v[72:75]
	v_mfma_f32_16x16x32_bf16 v[68:71], v[132:135], v[200:203], v[68:71]
	v_mfma_f32_16x16x32_bf16 v[64:67], v[140:143], v[200:203], v[64:67]
	s_setprio 0
	s_setprio 1
	v_mfma_f32_16x16x32_bf16 v[28:31], v[144:147], v[160:163], v[28:31]
	v_mfma_f32_16x16x32_bf16 v[24:27], v[152:155], v[160:163], v[24:27]
	v_mfma_f32_16x16x32_bf16 v[20:23], v[144:147], v[168:171], v[20:23]
	v_mfma_f32_16x16x32_bf16 v[16:19], v[152:155], v[168:171], v[16:19]
	v_mfma_f32_16x16x32_bf16 v[12:15], v[144:147], v[188:191], v[12:15]
	v_mfma_f32_16x16x32_bf16 v[8:11], v[152:155], v[188:191], v[8:11]
	v_mfma_f32_16x16x32_bf16 v[4:7], v[144:147], v[196:199], v[4:7]
	v_mfma_f32_16x16x32_bf16 v[0:3], v[152:155], v[196:199], v[0:3]
	v_mfma_f32_16x16x32_bf16 v[28:31], v[148:151], v[164:167], v[28:31]
	v_mfma_f32_16x16x32_bf16 v[24:27], v[156:159], v[164:167], v[24:27]
	v_mfma_f32_16x16x32_bf16 v[20:23], v[148:151], v[184:187], v[20:23]
	v_mfma_f32_16x16x32_bf16 v[16:19], v[156:159], v[184:187], v[16:19]
	v_mfma_f32_16x16x32_bf16 v[12:15], v[148:151], v[192:195], v[12:15]
	v_mfma_f32_16x16x32_bf16 v[8:11], v[156:159], v[192:195], v[8:11]
	v_mfma_f32_16x16x32_bf16 v[4:7], v[148:151], v[200:203], v[4:7]
	v_mfma_f32_16x16x32_bf16 v[0:3], v[156:159], v[200:203], v[0:3]
	s_setprio 0
	v_add_u32_e32 v140, s28, v215
	v_add_u32_e32 v156, s54, v215
	s_add_i32 s80, s80, 2
	s_add_u32 s49, s49, 0x10000
	s_addc_u32 s55, s55, 0
	s_add_u32 s0, s0, 0x100
	s_addc_u32 s1, s1, 0
	s_cmp_gt_u32 s80, 29
	s_barrier
.LBB0_1055:
	ds_read_b128 v[128:131], v140
	ds_read_b128 v[132:135], v140 offset:1024
	ds_read_b128 v[136:139], v140 offset:2048
	ds_read_b128 v[140:143], v140 offset:3072
	ds_read_b128 v[144:147], v156
	ds_read_b128 v[148:151], v156 offset:1024
	ds_read_b128 v[152:155], v156 offset:2048
	ds_read_b128 v[156:159], v156 offset:3072
	s_add_u32 s50, s0, 0xfff80080
	s_addc_u32 s51, s1, -1
	s_cmp_eq_u32 s80, 28
	s_cselect_b32 s53, s4, s51
	s_cselect_b32 s52, s5, s50
	s_cselect_b32 s51, s39, s55
	s_cselect_b32 s50, s41, s49
	v_lshl_add_u64 v[204:205], s[0:1], 0, v[180:181]
	s_add_i32 m0, s58, 0xc000
	ds_read_b128 v[160:163], v251
	ds_read_b128 v[164:167], v251 offset:1024
	ds_read_b128 v[168:171], v251 offset:2048
	ds_read_b128 v[184:187], v251 offset:3072
	ds_read_b128 v[188:191], v251 offset:4096
	ds_read_b128 v[192:195], v251 offset:5120
	ds_read_b128 v[196:199], v251 offset:6144
	ds_read_b128 v[200:203], v251 offset:7168
	global_load_lds_dwordx4 v[204:205], off
	v_lshl_add_u64 v[204:205], s[0:1], 0, v[182:183]
	s_add_i32 m0, s58, 0xe000
	s_nop 0
	global_load_lds_dwordx4 v[204:205], off
	s_waitcnt vmcnt(8)
	s_waitcnt lgkmcnt(0)
	s_barrier
	s_setprio 1
	s_waitcnt lgkmcnt(0)
	v_mfma_f32_16x16x32_bf16 v[124:127], v[128:131], v[160:163], v[124:127]
	v_mfma_f32_16x16x32_bf16 v[120:123], v[136:139], v[160:163], v[120:123]
	v_mfma_f32_16x16x32_bf16 v[116:119], v[128:131], v[168:171], v[116:119]
	v_mfma_f32_16x16x32_bf16 v[112:115], v[136:139], v[168:171], v[112:115]
	v_mfma_f32_16x16x32_bf16 v[108:111], v[128:131], v[188:191], v[108:111]
	v_mfma_f32_16x16x32_bf16 v[104:107], v[136:139], v[188:191], v[104:107]
	v_mfma_f32_16x16x32_bf16 v[100:103], v[128:131], v[196:199], v[100:103]
	v_mfma_f32_16x16x32_bf16 v[96:99], v[136:139], v[196:199], v[96:99]
	v_mfma_f32_16x16x32_bf16 v[124:127], v[132:135], v[164:167], v[124:127]
	v_mfma_f32_16x16x32_bf16 v[120:123], v[140:143], v[164:167], v[120:123]
	v_mfma_f32_16x16x32_bf16 v[116:119], v[132:135], v[184:187], v[116:119]
	v_mfma_f32_16x16x32_bf16 v[112:115], v[140:143], v[184:187], v[112:115]
	v_mfma_f32_16x16x32_bf16 v[108:111], v[132:135], v[192:195], v[108:111]
	v_mfma_f32_16x16x32_bf16 v[104:107], v[140:143], v[192:195], v[104:107]
	v_mfma_f32_16x16x32_bf16 v[100:103], v[132:135], v[200:203], v[100:103]
	v_mfma_f32_16x16x32_bf16 v[96:99], v[140:143], v[200:203], v[96:99]
	s_setprio 0
	s_setprio 1
	v_mfma_f32_16x16x32_bf16 v[60:63], v[144:147], v[160:163], v[60:63]
	v_mfma_f32_16x16x32_bf16 v[56:59], v[152:155], v[160:163], v[56:59]
	v_mfma_f32_16x16x32_bf16 v[52:55], v[144:147], v[168:171], v[52:55]
	v_mfma_f32_16x16x32_bf16 v[48:51], v[152:155], v[168:171], v[48:51]
	v_mfma_f32_16x16x32_bf16 v[44:47], v[144:147], v[188:191], v[44:47]
	v_mfma_f32_16x16x32_bf16 v[40:43], v[152:155], v[188:191], v[40:43]
	v_mfma_f32_16x16x32_bf16 v[36:39], v[144:147], v[196:199], v[36:39]
	v_mfma_f32_16x16x32_bf16 v[32:35], v[152:155], v[196:199], v[32:35]
	v_mfma_f32_16x16x32_bf16 v[60:63], v[148:151], v[164:167], v[60:63]
	v_mfma_f32_16x16x32_bf16 v[56:59], v[156:159], v[164:167], v[56:59]
	v_mfma_f32_16x16x32_bf16 v[52:55], v[148:151], v[184:187], v[52:55]
	v_mfma_f32_16x16x32_bf16 v[48:51], v[156:159], v[184:187], v[48:51]
	v_mfma_f32_16x16x32_bf16 v[44:47], v[148:151], v[192:195], v[44:47]
	v_mfma_f32_16x16x32_bf16 v[40:43], v[156:159], v[192:195], v[40:43]
	v_mfma_f32_16x16x32_bf16 v[36:39], v[148:151], v[200:203], v[36:39]
	v_mfma_f32_16x16x32_bf16 v[32:35], v[156:159], v[200:203], v[32:35]
	s_setprio 0
	s_barrier
	s_mov_b32 m0, s30
	v_lshl_add_u64 v[204:205], s[50:51], 0, v[174:175]
	s_add_u32 s82, s50, 0x4000
	ds_read_b128 v[160:163], v251 offset:16384
	ds_read_b128 v[164:167], v251 offset:17408
	ds_read_b128 v[168:171], v251 offset:18432
	ds_read_b128 v[184:187], v251 offset:19456
	ds_read_b128 v[188:191], v251 offset:20480
	ds_read_b128 v[192:195], v251 offset:21504
	ds_read_b128 v[196:199], v251 offset:22528
	ds_read_b128 v[200:203], v251 offset:23552
	global_load_lds_dwordx4 v[204:205], off
	v_lshl_add_u64 v[204:205], s[50:51], 0, v[178:179]
	s_mov_b32 m0, s43
	s_addc_u32 s83, s51, 0
	global_load_lds_dwordx4 v[204:205], off
	v_lshl_add_u64 v[204:205], s[82:83], 0, v[174:175]
	s_mov_b32 m0, s56
	v_lshl_add_u64 v[206:207], s[52:53], 0, v[176:177]
	global_load_lds_dwordx4 v[204:205], off
	v_lshl_add_u64 v[204:205], s[82:83], 0, v[178:179]
	s_mov_b32 m0, s57
	s_nop 0
	global_load_lds_dwordx4 v[204:205], off
	v_lshl_add_u64 v[204:205], s[52:53], 0, v[172:173]
	s_mov_b32 m0, s58
	s_nop 0
	global_load_lds_dwordx4 v[204:205], off
	s_mov_b32 m0, s59
	s_nop 0
	global_load_lds_dwordx4 v[206:207], off
	s_waitcnt vmcnt(8)
	s_waitcnt lgkmcnt(0)
	s_barrier
	s_setprio 1
	s_waitcnt lgkmcnt(0)
	v_mfma_f32_16x16x32_bf16 v[92:95], v[128:131], v[160:163], v[92:95]
	v_mfma_f32_16x16x32_bf16 v[88:91], v[136:139], v[160:163], v[88:91]
	v_mfma_f32_16x16x32_bf16 v[84:87], v[128:131], v[168:171], v[84:87]
	v_mfma_f32_16x16x32_bf16 v[80:83], v[136:139], v[168:171], v[80:83]
	v_mfma_f32_16x16x32_bf16 v[76:79], v[128:131], v[188:191], v[76:79]
	v_mfma_f32_16x16x32_bf16 v[72:75], v[136:139], v[188:191], v[72:75]
	v_mfma_f32_16x16x32_bf16 v[68:71], v[128:131], v[196:199], v[68:71]
	v_mfma_f32_16x16x32_bf16 v[64:67], v[136:139], v[196:199], v[64:67]
	v_mfma_f32_16x16x32_bf16 v[92:95], v[132:135], v[164:167], v[92:95]
	v_mfma_f32_16x16x32_bf16 v[88:91], v[140:143], v[164:167], v[88:91]
	v_mfma_f32_16x16x32_bf16 v[84:87], v[132:135], v[184:187], v[84:87]
	v_mfma_f32_16x16x32_bf16 v[80:83], v[140:143], v[184:187], v[80:83]
	v_mfma_f32_16x16x32_bf16 v[76:79], v[132:135], v[192:195], v[76:79]
	v_mfma_f32_16x16x32_bf16 v[72:75], v[140:143], v[192:195], v[72:75]
	v_mfma_f32_16x16x32_bf16 v[68:71], v[132:135], v[200:203], v[68:71]
	v_mfma_f32_16x16x32_bf16 v[64:67], v[140:143], v[200:203], v[64:67]
	s_setprio 0
	s_setprio 1
	v_mfma_f32_16x16x32_bf16 v[28:31], v[144:147], v[160:163], v[28:31]
	v_mfma_f32_16x16x32_bf16 v[24:27], v[152:155], v[160:163], v[24:27]
	v_mfma_f32_16x16x32_bf16 v[20:23], v[144:147], v[168:171], v[20:23]
	v_mfma_f32_16x16x32_bf16 v[16:19], v[152:155], v[168:171], v[16:19]
	v_mfma_f32_16x16x32_bf16 v[12:15], v[144:147], v[188:191], v[12:15]
	v_mfma_f32_16x16x32_bf16 v[8:11], v[152:155], v[188:191], v[8:11]
	v_mfma_f32_16x16x32_bf16 v[4:7], v[144:147], v[196:199], v[4:7]
	v_mfma_f32_16x16x32_bf16 v[0:3], v[152:155], v[196:199], v[0:3]
	v_mfma_f32_16x16x32_bf16 v[28:31], v[148:151], v[164:167], v[28:31]
	v_mfma_f32_16x16x32_bf16 v[24:27], v[156:159], v[164:167], v[24:27]
	v_mfma_f32_16x16x32_bf16 v[20:23], v[148:151], v[184:187], v[20:23]
	v_mfma_f32_16x16x32_bf16 v[16:19], v[156:159], v[184:187], v[16:19]
	v_mfma_f32_16x16x32_bf16 v[12:15], v[148:151], v[192:195], v[12:15]
	v_mfma_f32_16x16x32_bf16 v[8:11], v[156:159], v[192:195], v[8:11]
	v_mfma_f32_16x16x32_bf16 v[4:7], v[148:151], v[200:203], v[4:7]
	v_mfma_f32_16x16x32_bf16 v[0:3], v[156:159], v[200:203], v[0:3]
	s_setprio 0
	s_barrier
	v_add_u32_e32 v140, s68, v215
	v_add_u32_e32 v156, s73, v215
	ds_read_b128 v[128:131], v140
	ds_read_b128 v[132:135], v140 offset:1024
	ds_read_b128 v[136:139], v140 offset:2048
	ds_read_b128 v[140:143], v140 offset:3072
	ds_read_b128 v[144:147], v156
	ds_read_b128 v[148:151], v156 offset:1024
	ds_read_b128 v[152:155], v156 offset:2048
	ds_read_b128 v[156:159], v156 offset:3072
	s_add_u32 s52, s52, 0x80000
	s_addc_u32 s53, s53, 0
	s_mov_b32 m0, s60
	v_lshl_add_u64 v[208:209], s[52:53], 0, v[172:173]
	ds_read_b128 v[160:163], v251 offset:32768
	ds_read_b128 v[164:167], v251 offset:33792
	ds_read_b128 v[168:171], v251 offset:34816
	ds_read_b128 v[184:187], v251 offset:35840
	ds_read_b128 v[188:191], v251 offset:36864
	ds_read_b128 v[192:195], v251 offset:37888
	ds_read_b128 v[196:199], v251 offset:38912
	ds_read_b128 v[200:203], v251 offset:39936
	global_load_lds_dwordx4 v[208:209], off
	v_lshl_add_u64 v[208:209], s[52:53], 0, v[176:177]
	s_mov_b32 m0, s61
	s_nop 0
	global_load_lds_dwordx4 v[208:209], off
	s_waitcnt vmcnt(8)
	s_waitcnt lgkmcnt(0)
	s_barrier
	s_setprio 1
	s_waitcnt lgkmcnt(0)
	v_mfma_f32_16x16x32_bf16 v[124:127], v[128:131], v[160:163], v[124:127]
	v_mfma_f32_16x16x32_bf16 v[120:123], v[136:139], v[160:163], v[120:123]
	v_mfma_f32_16x16x32_bf16 v[116:119], v[128:131], v[168:171], v[116:119]
	v_mfma_f32_16x16x32_bf16 v[112:115], v[136:139], v[168:171], v[112:115]
	v_mfma_f32_16x16x32_bf16 v[108:111], v[128:131], v[188:191], v[108:111]
	v_mfma_f32_16x16x32_bf16 v[104:107], v[136:139], v[188:191], v[104:107]
	v_mfma_f32_16x16x32_bf16 v[100:103], v[128:131], v[196:199], v[100:103]
	v_mfma_f32_16x16x32_bf16 v[96:99], v[136:139], v[196:199], v[96:99]
	v_mfma_f32_16x16x32_bf16 v[124:127], v[132:135], v[164:167], v[124:127]
	v_mfma_f32_16x16x32_bf16 v[120:123], v[140:143], v[164:167], v[120:123]
	v_mfma_f32_16x16x32_bf16 v[116:119], v[132:135], v[184:187], v[116:119]
	v_mfma_f32_16x16x32_bf16 v[112:115], v[140:143], v[184:187], v[112:115]
	v_mfma_f32_16x16x32_bf16 v[108:111], v[132:135], v[192:195], v[108:111]
	v_mfma_f32_16x16x32_bf16 v[104:107], v[140:143], v[192:195], v[104:107]
	v_mfma_f32_16x16x32_bf16 v[100:103], v[132:135], v[200:203], v[100:103]
	v_mfma_f32_16x16x32_bf16 v[96:99], v[140:143], v[200:203], v[96:99]
	s_setprio 0
	s_setprio 1
	v_mfma_f32_16x16x32_bf16 v[60:63], v[144:147], v[160:163], v[60:63]
	v_mfma_f32_16x16x32_bf16 v[56:59], v[152:155], v[160:163], v[56:59]
	v_mfma_f32_16x16x32_bf16 v[52:55], v[144:147], v[168:171], v[52:55]
	v_mfma_f32_16x16x32_bf16 v[48:51], v[152:155], v[168:171], v[48:51]
	v_mfma_f32_16x16x32_bf16 v[44:47], v[144:147], v[188:191], v[44:47]
	v_mfma_f32_16x16x32_bf16 v[40:43], v[152:155], v[188:191], v[40:43]
	v_mfma_f32_16x16x32_bf16 v[36:39], v[144:147], v[196:199], v[36:39]
	v_mfma_f32_16x16x32_bf16 v[32:35], v[152:155], v[196:199], v[32:35]
	v_mfma_f32_16x16x32_bf16 v[60:63], v[148:151], v[164:167], v[60:63]
	v_mfma_f32_16x16x32_bf16 v[56:59], v[156:159], v[164:167], v[56:59]
	v_mfma_f32_16x16x32_bf16 v[52:55], v[148:151], v[184:187], v[52:55]
	v_mfma_f32_16x16x32_bf16 v[48:51], v[156:159], v[184:187], v[48:51]
	v_mfma_f32_16x16x32_bf16 v[44:47], v[148:151], v[192:195], v[44:47]
	v_mfma_f32_16x16x32_bf16 v[40:43], v[156:159], v[192:195], v[40:43]
	v_mfma_f32_16x16x32_bf16 v[36:39], v[148:151], v[200:203], v[36:39]
	v_mfma_f32_16x16x32_bf16 v[32:35], v[156:159], v[200:203], v[32:35]
	s_setprio 0
	s_barrier
	s_add_u32 s52, s50, 0x8000
	s_addc_u32 s53, s51, 0
	s_mov_b32 m0, s69
	v_lshl_add_u64 v[208:209], s[52:53], 0, v[174:175]
	s_add_u32 s50, s50, 0xc000
	ds_read_b128 v[160:163], v251 offset:49152
	ds_read_b128 v[164:167], v251 offset:50176
	ds_read_b128 v[168:171], v251 offset:51200
	ds_read_b128 v[184:187], v251 offset:52224
	ds_read_b128 v[188:191], v251 offset:53248
	ds_read_b128 v[192:195], v251 offset:54272
	ds_read_b128 v[196:199], v251 offset:55296
	ds_read_b128 v[200:203], v251 offset:56320
	global_load_lds_dwordx4 v[208:209], off
	v_lshl_add_u64 v[208:209], s[52:53], 0, v[178:179]
	s_mov_b32 m0, s70
	s_addc_u32 s51, s51, 0
	global_load_lds_dwordx4 v[208:209], off
	v_lshl_add_u64 v[208:209], s[50:51], 0, v[174:175]
	s_mov_b32 m0, s74
	v_lshl_add_u64 v[204:205], v[204:205], 0, s[26:27]
	global_load_lds_dwordx4 v[208:209], off
	v_lshl_add_u64 v[208:209], s[50:51], 0, v[178:179]
	s_mov_b32 m0, s75
	s_nop 0
	global_load_lds_dwordx4 v[208:209], off
	s_mov_b32 m0, s71
	s_nop 0
	global_load_lds_dwordx4 v[204:205], off
	v_lshl_add_u64 v[204:205], v[206:207], 0, s[26:27]
	s_mov_b32 m0, s72
	s_nop 0
	global_load_lds_dwordx4 v[204:205], off
	s_waitcnt vmcnt(8)
	s_waitcnt lgkmcnt(0)
	s_barrier
	s_setprio 1
	s_waitcnt lgkmcnt(0)
	v_mfma_f32_16x16x32_bf16 v[92:95], v[128:131], v[160:163], v[92:95]
	v_mfma_f32_16x16x32_bf16 v[88:91], v[136:139], v[160:163], v[88:91]
	v_mfma_f32_16x16x32_bf16 v[84:87], v[128:131], v[168:171], v[84:87]
	v_mfma_f32_16x16x32_bf16 v[80:83], v[136:139], v[168:171], v[80:83]
	v_mfma_f32_16x16x32_bf16 v[76:79], v[128:131], v[188:191], v[76:79]
	v_mfma_f32_16x16x32_bf16 v[72:75], v[136:139], v[188:191], v[72:75]
	v_mfma_f32_16x16x32_bf16 v[68:71], v[128:131], v[196:199], v[68:71]
	v_mfma_f32_16x16x32_bf16 v[64:67], v[136:139], v[196:199], v[64:67]
	v_mfma_f32_16x16x32_bf16 v[92:95], v[132:135], v[164:167], v[92:95]
	v_mfma_f32_16x16x32_bf16 v[88:91], v[140:143], v[164:167], v[88:91]
	v_mfma_f32_16x16x32_bf16 v[84:87], v[132:135], v[184:187], v[84:87]
	v_mfma_f32_16x16x32_bf16 v[80:83], v[140:143], v[184:187], v[80:83]
	v_mfma_f32_16x16x32_bf16 v[76:79], v[132:135], v[192:195], v[76:79]
	v_mfma_f32_16x16x32_bf16 v[72:75], v[140:143], v[192:195], v[72:75]
	v_mfma_f32_16x16x32_bf16 v[68:71], v[132:135], v[200:203], v[68:71]
	v_mfma_f32_16x16x32_bf16 v[64:67], v[140:143], v[200:203], v[64:67]
	s_setprio 0
	s_setprio 1
	v_mfma_f32_16x16x32_bf16 v[28:31], v[144:147], v[160:163], v[28:31]
	v_mfma_f32_16x16x32_bf16 v[24:27], v[152:155], v[160:163], v[24:27]
	v_mfma_f32_16x16x32_bf16 v[20:23], v[144:147], v[168:171], v[20:23]
	v_mfma_f32_16x16x32_bf16 v[16:19], v[152:155], v[168:171], v[16:19]
	v_mfma_f32_16x16x32_bf16 v[12:15], v[144:147], v[188:191], v[12:15]
	v_mfma_f32_16x16x32_bf16 v[8:11], v[152:155], v[188:191], v[8:11]
	v_mfma_f32_16x16x32_bf16 v[4:7], v[144:147], v[196:199], v[4:7]
	v_mfma_f32_16x16x32_bf16 v[0:3], v[152:155], v[196:199], v[0:3]
	v_mfma_f32_16x16x32_bf16 v[28:31], v[148:151], v[164:167], v[28:31]
	v_mfma_f32_16x16x32_bf16 v[24:27], v[156:159], v[164:167], v[24:27]
	v_mfma_f32_16x16x32_bf16 v[20:23], v[148:151], v[184:187], v[20:23]
	v_mfma_f32_16x16x32_bf16 v[16:19], v[156:159], v[184:187], v[16:19]
	v_mfma_f32_16x16x32_bf16 v[12:15], v[148:151], v[192:195], v[12:15]
	v_mfma_f32_16x16x32_bf16 v[8:11], v[156:159], v[192:195], v[8:11]
	v_mfma_f32_16x16x32_bf16 v[4:7], v[148:151], v[200:203], v[4:7]
	v_mfma_f32_16x16x32_bf16 v[0:3], v[156:159], v[200:203], v[0:3]
	s_setprio 0
	v_add_u32_e32 v140, s28, v215
	v_add_u32_e32 v156, s54, v215
	s_add_i32 s80, s80, 2
	s_add_u32 s49, s49, 0x10000
	s_addc_u32 s55, s55, 0
	s_add_u32 s0, s0, 0x100
	s_addc_u32 s1, s1, 0
	s_cmp_gt_u32 s80, 29
	s_barrier
	s_cbranch_scc0 .LBB0_1055
	v_mov_b64_e32 v[220:221], 0x1ff
	v_mov_b64_e32 v[218:219], 0x200
	s_and_b64 vcc, exec, s[34:35]
	s_cbranch_vccz .LBB0_1058
	s_barrier

.LBB0_1139:
	s_and_saveexec_b64 s[4:5], s[0:1]
	s_cbranch_execz .LBB0_1141
	s_ashr_i32 s24, s28, 31
	s_lshr_b32 s24, s24, 28
	s_add_i32 s24, s28, s24
	s_ashr_i32 s24, s24, 4
	v_readlane_b32 s28, v255, 19
	s_ashr_i32 s25, s24, 31
	s_lshl_b32 s30, s28, 8
	s_ashr_i32 s31, s30, 31
	s_lshl_b64 s[24:25], s[24:25], 15
	s_add_u32 s28, s18, s24
	s_addc_u32 s38, s19, s25
	s_lshl_b64 s[24:25], s[30:31], 2
	s_add_u32 s24, s28, s24
	s_addc_u32 s25, s38, s25
	v_lshl_add_u64 v[8:9], v[0:1], 2, s[24:25]
	v_readfirstlane_b32 s24, v4
	s_mov_b32 m0, s24
	s_nop 0
	global_load_lds_dword v[8:9], off

.LBB0_1142:
	s_add_i32 s4, s16, 1
	s_cmp_lt_u32 s16, 7
	s_cselect_b64 s[24:25], -1, 0
	s_and_b64 s[24:25], s[36:37], s[24:25]
	s_add_u32 s20, s20, s13
	v_add_u32_e32 v6, 0x400, v6
	v_add_u32_e32 v4, 0x400, v4
	s_addc_u32 s21, s21, s15
	s_and_b64 vcc, exec, s[24:25]
	s_cbranch_vccnz .LBB0_1130
	v_mov_b32_e32 v3, -1
	v_lshl_add_u32 v1, v0, 2, s35
	s_mov_b32 s16, 0
	v_mov_b32_e32 v2, 0
	s_mov_b64 s[20:21], s[2:3]
	v_mov_b32_e32 v4, v3
	s_waitcnt vmcnt(0) lgkmcnt(0)
	s_barrier

.LBB0_1172:
	s_ashr_i32 s39, s38, 31
	s_lshl_b64 s[4:5], s[38:39], 20
	s_add_u32 s40, s18, s4
	s_addc_u32 s41, s19, s5
	s_and_b64 s[4:5], s[36:37], exec
	s_cselect_b32 s4, s41, s1
	s_cselect_b32 s5, s40, s0
	s_ashr_i32 s35, s34, 31
	s_lshl_b64 s[42:43], s[34:35], 20
	s_add_u32 s42, s16, s42
	s_addc_u32 s43, s17, s43
	s_and_b64 s[48:49], s[36:37], exec
	s_cselect_b32 s35, s43, s47
	s_cselect_b32 s39, s42, s46
	s_add_u32 s76, s46, 0x10000
	s_addc_u32 s77, s47, 0
	s_mov_b32 s78, -2
	v_add_u32_e32 v124, s28, v156
	v_add_u32_e32 v170, s45, v156
	ds_read_b128 v[108:111], v124
	ds_read_b128 v[112:115], v124 offset:1024
	ds_read_b128 v[120:123], v124 offset:2048
	ds_read_b128 v[124:127], v124 offset:3072
	ds_read_b128 v[158:161], v170
	ds_read_b128 v[162:165], v170 offset:1024
	ds_read_b128 v[166:169], v170 offset:2048
	ds_read_b128 v[170:173], v170 offset:3072
	s_add_u32 s46, s0, 0x10000
	s_addc_u32 s47, s1, 0
	s_cmp_eq_u32 s78, 28
	s_cselect_b32 s52, s5, s46
	s_cselect_b32 s53, s4, s47
	s_cselect_b32 s50, s39, s76
	s_cselect_b32 s51, s35, s77
	s_add_u32 s48, s52, 0x8000
	s_addc_u32 s49, s53, 0
	v_lshl_add_u64 v[206:207], s[0:1], 0, v[152:153]
	s_add_i32 m0, s56, 0xc000
	ds_read_b128 v[174:177], v157
	ds_read_b128 v[178:181], v157 offset:1024
	ds_read_b128 v[182:185], v157 offset:2048
	ds_read_b128 v[186:189], v157 offset:3072
	ds_read_b128 v[190:193], v157 offset:4096
	ds_read_b128 v[194:197], v157 offset:5120
	ds_read_b128 v[198:201], v157 offset:6144
	ds_read_b128 v[202:205], v157 offset:7168
	global_load_lds_dwordx4 v[206:207], off
	v_lshl_add_u64 v[206:207], s[0:1], 0, v[154:155]
	s_add_i32 m0, s56, 0xe000
	s_nop 0
	global_load_lds_dwordx4 v[206:207], off
	s_waitcnt vmcnt(8)
	s_waitcnt lgkmcnt(0)
	s_barrier
	s_setprio 1
	s_waitcnt lgkmcnt(0)
	v_mfma_f32_16x16x32_bf16 v[140:143], v[108:111], v[174:177], 0
	v_mfma_f32_16x16x32_bf16 v[136:139], v[120:123], v[174:177], 0
	v_mfma_f32_16x16x32_bf16 v[116:119], v[108:111], v[182:185], 0
	v_mfma_f32_16x16x32_bf16 v[104:107], v[120:123], v[182:185], 0
	v_mfma_f32_16x16x32_bf16 v[92:95], v[108:111], v[190:193], 0
	v_mfma_f32_16x16x32_bf16 v[88:91], v[120:123], v[190:193], 0
	v_mfma_f32_16x16x32_bf16 v[76:79], v[108:111], v[198:201], 0
	v_mfma_f32_16x16x32_bf16 v[72:75], v[120:123], v[198:201], 0
	v_mfma_f32_16x16x32_bf16 v[140:143], v[112:115], v[178:181], v[140:143]
	v_mfma_f32_16x16x32_bf16 v[136:139], v[124:127], v[178:181], v[136:139]
	v_mfma_f32_16x16x32_bf16 v[116:119], v[112:115], v[186:189], v[116:119]
	v_mfma_f32_16x16x32_bf16 v[104:107], v[124:127], v[186:189], v[104:107]
	v_mfma_f32_16x16x32_bf16 v[92:95], v[112:115], v[194:197], v[92:95]
	v_mfma_f32_16x16x32_bf16 v[88:91], v[124:127], v[194:197], v[88:91]
	v_mfma_f32_16x16x32_bf16 v[76:79], v[112:115], v[202:205], v[76:79]
	v_mfma_f32_16x16x32_bf16 v[72:75], v[124:127], v[202:205], v[72:75]
	s_setprio 0
	s_setprio 1
	v_mfma_f32_16x16x32_bf16 v[132:135], v[158:161], v[174:177], 0
	v_mfma_f32_16x16x32_bf16 v[128:131], v[166:169], v[174:177], 0
	v_mfma_f32_16x16x32_bf16 v[100:103], v[158:161], v[182:185], 0
	v_mfma_f32_16x16x32_bf16 v[96:99], v[166:169], v[182:185], 0
	v_mfma_f32_16x16x32_bf16 v[84:87], v[158:161], v[190:193], 0
	v_mfma_f32_16x16x32_bf16 v[80:83], v[166:169], v[190:193], 0
	v_mfma_f32_16x16x32_bf16 v[68:71], v[158:161], v[198:201], 0
	v_mfma_f32_16x16x32_bf16 v[64:67], v[166:169], v[198:201], 0
	v_mfma_f32_16x16x32_bf16 v[132:135], v[162:165], v[178:181], v[132:135]
	v_mfma_f32_16x16x32_bf16 v[128:131], v[170:173], v[178:181], v[128:131]
	v_mfma_f32_16x16x32_bf16 v[100:103], v[162:165], v[186:189], v[100:103]
	v_mfma_f32_16x16x32_bf16 v[96:99], v[170:173], v[186:189], v[96:99]
	v_mfma_f32_16x16x32_bf16 v[84:87], v[162:165], v[194:197], v[84:87]
	v_mfma_f32_16x16x32_bf16 v[80:83], v[170:173], v[194:197], v[80:83]
	v_mfma_f32_16x16x32_bf16 v[68:71], v[162:165], v[202:205], v[68:71]
	v_mfma_f32_16x16x32_bf16 v[64:67], v[170:173], v[202:205], v[64:67]
	s_setprio 0
	s_barrier
	s_mov_b32 m0, s30
	v_lshl_add_u64 v[206:207], s[50:51], 0, v[146:147]
	s_add_u32 s0, s50, 0x4000
	ds_read_b128 v[174:177], v157 offset:16384
	ds_read_b128 v[178:181], v157 offset:17408
	ds_read_b128 v[182:185], v157 offset:18432
	ds_read_b128 v[186:189], v157 offset:19456
	ds_read_b128 v[190:193], v157 offset:20480
	ds_read_b128 v[194:197], v157 offset:21504
	ds_read_b128 v[198:201], v157 offset:22528
	ds_read_b128 v[202:205], v157 offset:23552
	global_load_lds_dwordx4 v[206:207], off
	v_lshl_add_u64 v[206:207], s[50:51], 0, v[150:151]
	s_mov_b32 m0, s31
	s_addc_u32 s1, s51, 0
	global_load_lds_dwordx4 v[206:207], off
	v_lshl_add_u64 v[206:207], s[0:1], 0, v[146:147]
	s_mov_b32 m0, s54
	s_nop 0
	global_load_lds_dwordx4 v[206:207], off
	v_lshl_add_u64 v[206:207], s[0:1], 0, v[150:151]
	s_mov_b32 m0, s55
	s_nop 0
	global_load_lds_dwordx4 v[206:207], off
	v_lshl_add_u64 v[206:207], s[52:53], 0, v[144:145]
	s_mov_b32 m0, s56
	s_nop 0
	global_load_lds_dwordx4 v[206:207], off
	v_lshl_add_u64 v[206:207], s[52:53], 0, v[148:149]
	s_mov_b32 m0, s57
	s_nop 0
	global_load_lds_dwordx4 v[206:207], off
	s_waitcnt vmcnt(8)
	s_waitcnt lgkmcnt(0)
	s_barrier
	s_setprio 1
	s_waitcnt lgkmcnt(0)
	v_mfma_f32_16x16x32_bf16 v[60:63], v[108:111], v[174:177], 0
	v_mfma_f32_16x16x32_bf16 v[56:59], v[120:123], v[174:177], 0
	v_mfma_f32_16x16x32_bf16 v[44:47], v[108:111], v[182:185], 0
	v_mfma_f32_16x16x32_bf16 v[40:43], v[120:123], v[182:185], 0
	v_mfma_f32_16x16x32_bf16 v[28:31], v[108:111], v[190:193], 0
	v_mfma_f32_16x16x32_bf16 v[24:27], v[120:123], v[190:193], 0
	v_mfma_f32_16x16x32_bf16 v[12:15], v[108:111], v[198:201], 0
	v_mfma_f32_16x16x32_bf16 v[8:11], v[120:123], v[198:201], 0
	v_mfma_f32_16x16x32_bf16 v[60:63], v[112:115], v[178:181], v[60:63]
	v_mfma_f32_16x16x32_bf16 v[56:59], v[124:127], v[178:181], v[56:59]
	v_mfma_f32_16x16x32_bf16 v[44:47], v[112:115], v[186:189], v[44:47]
	v_mfma_f32_16x16x32_bf16 v[40:43], v[124:127], v[186:189], v[40:43]
	v_mfma_f32_16x16x32_bf16 v[28:31], v[112:115], v[194:197], v[28:31]
	v_mfma_f32_16x16x32_bf16 v[24:27], v[124:127], v[194:197], v[24:27]
	v_mfma_f32_16x16x32_bf16 v[12:15], v[112:115], v[202:205], v[12:15]
	v_mfma_f32_16x16x32_bf16 v[8:11], v[124:127], v[202:205], v[8:11]
	s_setprio 0
	s_setprio 1
	v_mfma_f32_16x16x32_bf16 v[52:55], v[158:161], v[174:177], 0
	v_mfma_f32_16x16x32_bf16 v[48:51], v[166:169], v[174:177], 0
	v_mfma_f32_16x16x32_bf16 v[36:39], v[158:161], v[182:185], 0
	v_mfma_f32_16x16x32_bf16 v[32:35], v[166:169], v[182:185], 0
	v_mfma_f32_16x16x32_bf16 v[20:23], v[158:161], v[190:193], 0
	v_mfma_f32_16x16x32_bf16 v[16:19], v[166:169], v[190:193], 0
	v_mfma_f32_16x16x32_bf16 v[4:7], v[158:161], v[198:201], 0
	v_mfma_f32_16x16x32_bf16 v[0:3], v[166:169], v[198:201], 0
	v_mfma_f32_16x16x32_bf16 v[52:55], v[162:165], v[178:181], v[52:55]
	v_mfma_f32_16x16x32_bf16 v[48:51], v[170:173], v[178:181], v[48:51]
	v_mfma_f32_16x16x32_bf16 v[36:39], v[162:165], v[186:189], v[36:39]
	v_mfma_f32_16x16x32_bf16 v[32:35], v[170:173], v[186:189], v[32:35]
	v_mfma_f32_16x16x32_bf16 v[20:23], v[162:165], v[194:197], v[20:23]
	v_mfma_f32_16x16x32_bf16 v[16:19], v[170:173], v[194:197], v[16:19]
	v_mfma_f32_16x16x32_bf16 v[4:7], v[162:165], v[202:205], v[4:7]
	v_mfma_f32_16x16x32_bf16 v[0:3], v[170:173], v[202:205], v[0:3]
	s_setprio 0
	s_barrier
	v_add_u32_e32 v124, s62, v156
	v_add_u32_e32 v170, s67, v156
	ds_read_b128 v[108:111], v124
	ds_read_b128 v[112:115], v124 offset:1024
	ds_read_b128 v[120:123], v124 offset:2048
	ds_read_b128 v[124:127], v124 offset:3072
	ds_read_b128 v[158:161], v170
	ds_read_b128 v[162:165], v170 offset:1024
	ds_read_b128 v[166:169], v170 offset:2048
	ds_read_b128 v[170:173], v170 offset:3072
	s_add_u32 s0, s52, 0x4000
	s_addc_u32 s1, s53, 0
	s_mov_b32 m0, s58
	v_lshl_add_u64 v[206:207], s[0:1], 0, v[144:145]
	ds_read_b128 v[174:177], v157 offset:32768
	ds_read_b128 v[178:181], v157 offset:33792
	ds_read_b128 v[182:185], v157 offset:34816
	ds_read_b128 v[186:189], v157 offset:35840
	ds_read_b128 v[190:193], v157 offset:36864
	ds_read_b128 v[194:197], v157 offset:37888
	ds_read_b128 v[198:201], v157 offset:38912
	ds_read_b128 v[202:205], v157 offset:39936
	global_load_lds_dwordx4 v[206:207], off
	v_lshl_add_u64 v[206:207], s[0:1], 0, v[148:149]
	s_mov_b32 m0, s59
	s_nop 0
	global_load_lds_dwordx4 v[206:207], off
	s_waitcnt vmcnt(8)
	s_waitcnt lgkmcnt(0)
	s_barrier
	s_setprio 1
	s_waitcnt lgkmcnt(0)
	v_mfma_f32_16x16x32_bf16 v[140:143], v[108:111], v[174:177], v[140:143]
	v_mfma_f32_16x16x32_bf16 v[136:139], v[120:123], v[174:177], v[136:139]
	v_mfma_f32_16x16x32_bf16 v[116:119], v[108:111], v[182:185], v[116:119]
	v_mfma_f32_16x16x32_bf16 v[104:107], v[120:123], v[182:185], v[104:107]
	v_mfma_f32_16x16x32_bf16 v[92:95], v[108:111], v[190:193], v[92:95]
	v_mfma_f32_16x16x32_bf16 v[88:91], v[120:123], v[190:193], v[88:91]
	v_mfma_f32_16x16x32_bf16 v[76:79], v[108:111], v[198:201], v[76:79]
	v_mfma_f32_16x16x32_bf16 v[72:75], v[120:123], v[198:201], v[72:75]
	v_mfma_f32_16x16x32_bf16 v[140:143], v[112:115], v[178:181], v[140:143]
	v_mfma_f32_16x16x32_bf16 v[136:139], v[124:127], v[178:181], v[136:139]
	v_mfma_f32_16x16x32_bf16 v[116:119], v[112:115], v[186:189], v[116:119]
	v_mfma_f32_16x16x32_bf16 v[104:107], v[124:127], v[186:189], v[104:107]
	v_mfma_f32_16x16x32_bf16 v[92:95], v[112:115], v[194:197], v[92:95]
	v_mfma_f32_16x16x32_bf16 v[88:91], v[124:127], v[194:197], v[88:91]
	v_mfma_f32_16x16x32_bf16 v[76:79], v[112:115], v[202:205], v[76:79]
	v_mfma_f32_16x16x32_bf16 v[72:75], v[124:127], v[202:205], v[72:75]
	s_setprio 0
	s_setprio 1
	v_mfma_f32_16x16x32_bf16 v[132:135], v[158:161], v[174:177], v[132:135]
	v_mfma_f32_16x16x32_bf16 v[128:131], v[166:169], v[174:177], v[128:131]
	v_mfma_f32_16x16x32_bf16 v[100:103], v[158:161], v[182:185], v[100:103]
	v_mfma_f32_16x16x32_bf16 v[96:99], v[166:169], v[182:185], v[96:99]
	v_mfma_f32_16x16x32_bf16 v[84:87], v[158:161], v[190:193], v[84:87]
	v_mfma_f32_16x16x32_bf16 v[80:83], v[166:169], v[190:193], v[80:83]
	v_mfma_f32_16x16x32_bf16 v[68:71], v[158:161], v[198:201], v[68:71]
	v_mfma_f32_16x16x32_bf16 v[64:67], v[166:169], v[198:201], v[64:67]
	v_mfma_f32_16x16x32_bf16 v[132:135], v[162:165], v[178:181], v[132:135]
	v_mfma_f32_16x16x32_bf16 v[128:131], v[170:173], v[178:181], v[128:131]
	v_mfma_f32_16x16x32_bf16 v[100:103], v[162:165], v[186:189], v[100:103]
	v_mfma_f32_16x16x32_bf16 v[96:99], v[170:173], v[186:189], v[96:99]
	v_mfma_f32_16x16x32_bf16 v[84:87], v[162:165], v[194:197], v[84:87]
	v_mfma_f32_16x16x32_bf16 v[80:83], v[170:173], v[194:197], v[80:83]
	v_mfma_f32_16x16x32_bf16 v[68:71], v[162:165], v[202:205], v[68:71]
	v_mfma_f32_16x16x32_bf16 v[64:67], v[170:173], v[202:205], v[64:67]
	s_setprio 0
	s_barrier
	s_add_u32 s0, s50, 0x8000
	s_addc_u32 s1, s51, 0
	s_mov_b32 m0, s63
	v_lshl_add_u64 v[206:207], s[0:1], 0, v[146:147]
	ds_read_b128 v[174:177], v157 offset:49152
	ds_read_b128 v[178:181], v157 offset:50176
	ds_read_b128 v[182:185], v157 offset:51200
	ds_read_b128 v[186:189], v157 offset:52224
	ds_read_b128 v[190:193], v157 offset:53248
	ds_read_b128 v[194:197], v157 offset:54272
	ds_read_b128 v[198:201], v157 offset:55296
	ds_read_b128 v[202:205], v157 offset:56320
	global_load_lds_dwordx4 v[206:207], off
	v_lshl_add_u64 v[206:207], s[0:1], 0, v[150:151]
	s_add_u32 s0, s50, 0xc000
	s_mov_b32 m0, s64
	s_addc_u32 s1, s51, 0
	global_load_lds_dwordx4 v[206:207], off
	v_lshl_add_u64 v[206:207], s[0:1], 0, v[146:147]
	s_mov_b32 m0, s68
	s_nop 0
	global_load_lds_dwordx4 v[206:207], off
	v_lshl_add_u64 v[206:207], s[0:1], 0, v[150:151]
	s_mov_b32 m0, s69
	s_nop 0
	global_load_lds_dwordx4 v[206:207], off
	v_lshl_add_u64 v[206:207], s[48:49], 0, v[144:145]
	s_mov_b32 m0, s65
	s_nop 0
	global_load_lds_dwordx4 v[206:207], off
	v_lshl_add_u64 v[206:207], s[48:49], 0, v[148:149]
	s_mov_b32 m0, s66
	s_nop 0
	global_load_lds_dwordx4 v[206:207], off
	s_waitcnt vmcnt(8)
	s_waitcnt lgkmcnt(0)
	s_barrier
	s_setprio 1
	s_waitcnt lgkmcnt(0)
	v_mfma_f32_16x16x32_bf16 v[60:63], v[108:111], v[174:177], v[60:63]
	v_mfma_f32_16x16x32_bf16 v[56:59], v[120:123], v[174:177], v[56:59]
	v_mfma_f32_16x16x32_bf16 v[44:47], v[108:111], v[182:185], v[44:47]
	v_mfma_f32_16x16x32_bf16 v[40:43], v[120:123], v[182:185], v[40:43]
	v_mfma_f32_16x16x32_bf16 v[28:31], v[108:111], v[190:193], v[28:31]
	v_mfma_f32_16x16x32_bf16 v[24:27], v[120:123], v[190:193], v[24:27]
	v_mfma_f32_16x16x32_bf16 v[12:15], v[108:111], v[198:201], v[12:15]
	v_mfma_f32_16x16x32_bf16 v[8:11], v[120:123], v[198:201], v[8:11]
	v_mfma_f32_16x16x32_bf16 v[60:63], v[112:115], v[178:181], v[60:63]
	v_mfma_f32_16x16x32_bf16 v[56:59], v[124:127], v[178:181], v[56:59]
	v_mfma_f32_16x16x32_bf16 v[44:47], v[112:115], v[186:189], v[44:47]
	v_mfma_f32_16x16x32_bf16 v[40:43], v[124:127], v[186:189], v[40:43]
	v_mfma_f32_16x16x32_bf16 v[28:31], v[112:115], v[194:197], v[28:31]
	v_mfma_f32_16x16x32_bf16 v[24:27], v[124:127], v[194:197], v[24:27]
	v_mfma_f32_16x16x32_bf16 v[12:15], v[112:115], v[202:205], v[12:15]
	v_mfma_f32_16x16x32_bf16 v[8:11], v[124:127], v[202:205], v[8:11]
	s_setprio 0
	s_setprio 1
	v_mfma_f32_16x16x32_bf16 v[52:55], v[158:161], v[174:177], v[52:55]
	v_mfma_f32_16x16x32_bf16 v[48:51], v[166:169], v[174:177], v[48:51]
	v_mfma_f32_16x16x32_bf16 v[36:39], v[158:161], v[182:185], v[36:39]
	v_mfma_f32_16x16x32_bf16 v[32:35], v[166:169], v[182:185], v[32:35]
	v_mfma_f32_16x16x32_bf16 v[20:23], v[158:161], v[190:193], v[20:23]
	v_mfma_f32_16x16x32_bf16 v[16:19], v[166:169], v[190:193], v[16:19]
	v_mfma_f32_16x16x32_bf16 v[4:7], v[158:161], v[198:201], v[4:7]
	v_mfma_f32_16x16x32_bf16 v[0:3], v[166:169], v[198:201], v[0:3]
	v_mfma_f32_16x16x32_bf16 v[52:55], v[162:165], v[178:181], v[52:55]
	v_mfma_f32_16x16x32_bf16 v[48:51], v[170:173], v[178:181], v[48:51]
	v_mfma_f32_16x16x32_bf16 v[36:39], v[162:165], v[186:189], v[36:39]
	v_mfma_f32_16x16x32_bf16 v[32:35], v[170:173], v[186:189], v[32:35]
	v_mfma_f32_16x16x32_bf16 v[20:23], v[162:165], v[194:197], v[20:23]
	v_mfma_f32_16x16x32_bf16 v[16:19], v[170:173], v[194:197], v[16:19]
	v_mfma_f32_16x16x32_bf16 v[4:7], v[162:165], v[202:205], v[4:7]
	v_mfma_f32_16x16x32_bf16 v[0:3], v[170:173], v[202:205], v[0:3]
	s_setprio 0
	v_add_u32_e32 v124, s28, v156
	v_add_u32_e32 v170, s45, v156
	s_add_i32 s78, s78, 2
	s_add_u32 s76, s76, 0x10000
	s_addc_u32 s77, s77, 0
	s_mov_b64 s[0:1], s[46:47]
	s_cmp_gt_u32 s78, 29
	s_barrier
.LBB0_1173:
	ds_read_b128 v[108:111], v124
	ds_read_b128 v[112:115], v124 offset:1024
	ds_read_b128 v[120:123], v124 offset:2048
	ds_read_b128 v[124:127], v124 offset:3072
	ds_read_b128 v[158:161], v170
	ds_read_b128 v[162:165], v170 offset:1024
	ds_read_b128 v[166:169], v170 offset:2048
	ds_read_b128 v[170:173], v170 offset:3072
	s_add_u32 s46, s0, 0x10000
	s_addc_u32 s47, s1, 0
	s_cmp_eq_u32 s78, 28
	s_cselect_b32 s52, s5, s46
	s_cselect_b32 s53, s4, s47
	s_cselect_b32 s50, s39, s76
	s_cselect_b32 s51, s35, s77
	s_add_u32 s48, s52, 0x8000
	s_addc_u32 s49, s53, 0
	v_lshl_add_u64 v[206:207], s[0:1], 0, v[152:153]
	s_add_i32 m0, s56, 0xc000
	ds_read_b128 v[174:177], v157
	ds_read_b128 v[178:181], v157 offset:1024
	ds_read_b128 v[182:185], v157 offset:2048
	ds_read_b128 v[186:189], v157 offset:3072
	ds_read_b128 v[190:193], v157 offset:4096
	ds_read_b128 v[194:197], v157 offset:5120
	ds_read_b128 v[198:201], v157 offset:6144
	ds_read_b128 v[202:205], v157 offset:7168
	global_load_lds_dwordx4 v[206:207], off
	v_lshl_add_u64 v[206:207], s[0:1], 0, v[154:155]
	s_add_i32 m0, s56, 0xe000
	s_nop 0
	global_load_lds_dwordx4 v[206:207], off
	s_waitcnt vmcnt(8)
	s_waitcnt lgkmcnt(0)
	s_barrier
	s_setprio 1
	s_waitcnt lgkmcnt(0)
	v_mfma_f32_16x16x32_bf16 v[140:143], v[108:111], v[174:177], v[140:143]
	v_mfma_f32_16x16x32_bf16 v[136:139], v[120:123], v[174:177], v[136:139]
	v_mfma_f32_16x16x32_bf16 v[116:119], v[108:111], v[182:185], v[116:119]
	v_mfma_f32_16x16x32_bf16 v[104:107], v[120:123], v[182:185], v[104:107]
	v_mfma_f32_16x16x32_bf16 v[92:95], v[108:111], v[190:193], v[92:95]
	v_mfma_f32_16x16x32_bf16 v[88:91], v[120:123], v[190:193], v[88:91]
	v_mfma_f32_16x16x32_bf16 v[76:79], v[108:111], v[198:201], v[76:79]
	v_mfma_f32_16x16x32_bf16 v[72:75], v[120:123], v[198:201], v[72:75]
	v_mfma_f32_16x16x32_bf16 v[140:143], v[112:115], v[178:181], v[140:143]
	v_mfma_f32_16x16x32_bf16 v[136:139], v[124:127], v[178:181], v[136:139]
	v_mfma_f32_16x16x32_bf16 v[116:119], v[112:115], v[186:189], v[116:119]
	v_mfma_f32_16x16x32_bf16 v[104:107], v[124:127], v[186:189], v[104:107]
	v_mfma_f32_16x16x32_bf16 v[92:95], v[112:115], v[194:197], v[92:95]
	v_mfma_f32_16x16x32_bf16 v[88:91], v[124:127], v[194:197], v[88:91]
	v_mfma_f32_16x16x32_bf16 v[76:79], v[112:115], v[202:205], v[76:79]
	v_mfma_f32_16x16x32_bf16 v[72:75], v[124:127], v[202:205], v[72:75]
	s_setprio 0
	s_setprio 1
	v_mfma_f32_16x16x32_bf16 v[132:135], v[158:161], v[174:177], v[132:135]
	v_mfma_f32_16x16x32_bf16 v[128:131], v[166:169], v[174:177], v[128:131]
	v_mfma_f32_16x16x32_bf16 v[100:103], v[158:161], v[182:185], v[100:103]
	v_mfma_f32_16x16x32_bf16 v[96:99], v[166:169], v[182:185], v[96:99]
	v_mfma_f32_16x16x32_bf16 v[84:87], v[158:161], v[190:193], v[84:87]
	v_mfma_f32_16x16x32_bf16 v[80:83], v[166:169], v[190:193], v[80:83]
	v_mfma_f32_16x16x32_bf16 v[68:71], v[158:161], v[198:201], v[68:71]
	v_mfma_f32_16x16x32_bf16 v[64:67], v[166:169], v[198:201], v[64:67]
	v_mfma_f32_16x16x32_bf16 v[132:135], v[162:165], v[178:181], v[132:135]
	v_mfma_f32_16x16x32_bf16 v[128:131], v[170:173], v[178:181], v[128:131]
	v_mfma_f32_16x16x32_bf16 v[100:103], v[162:165], v[186:189], v[100:103]
	v_mfma_f32_16x16x32_bf16 v[96:99], v[170:173], v[186:189], v[96:99]
	v_mfma_f32_16x16x32_bf16 v[84:87], v[162:165], v[194:197], v[84:87]
	v_mfma_f32_16x16x32_bf16 v[80:83], v[170:173], v[194:197], v[80:83]
	v_mfma_f32_16x16x32_bf16 v[68:71], v[162:165], v[202:205], v[68:71]
	v_mfma_f32_16x16x32_bf16 v[64:67], v[170:173], v[202:205], v[64:67]
	s_setprio 0
	s_barrier
	s_mov_b32 m0, s30
	v_lshl_add_u64 v[206:207], s[50:51], 0, v[146:147]
	s_add_u32 s0, s50, 0x4000
	ds_read_b128 v[174:177], v157 offset:16384
	ds_read_b128 v[178:181], v157 offset:17408
	ds_read_b128 v[182:185], v157 offset:18432
	ds_read_b128 v[186:189], v157 offset:19456
	ds_read_b128 v[190:193], v157 offset:20480
	ds_read_b128 v[194:197], v157 offset:21504
	ds_read_b128 v[198:201], v157 offset:22528
	ds_read_b128 v[202:205], v157 offset:23552
	global_load_lds_dwordx4 v[206:207], off
	v_lshl_add_u64 v[206:207], s[50:51], 0, v[150:151]
	s_mov_b32 m0, s31
	s_addc_u32 s1, s51, 0
	global_load_lds_dwordx4 v[206:207], off
	v_lshl_add_u64 v[206:207], s[0:1], 0, v[146:147]
	s_mov_b32 m0, s54
	s_nop 0
	global_load_lds_dwordx4 v[206:207], off
	v_lshl_add_u64 v[206:207], s[0:1], 0, v[150:151]
	s_mov_b32 m0, s55
	s_nop 0
	global_load_lds_dwordx4 v[206:207], off
	v_lshl_add_u64 v[206:207], s[52:53], 0, v[144:145]
	s_mov_b32 m0, s56
	s_nop 0
	global_load_lds_dwordx4 v[206:207], off
	v_lshl_add_u64 v[206:207], s[52:53], 0, v[148:149]
	s_mov_b32 m0, s57
	s_nop 0
	global_load_lds_dwordx4 v[206:207], off
	s_waitcnt vmcnt(8)
	s_waitcnt lgkmcnt(0)
	s_barrier
	s_setprio 1
	s_waitcnt lgkmcnt(0)
	v_mfma_f32_16x16x32_bf16 v[60:63], v[108:111], v[174:177], v[60:63]
	v_mfma_f32_16x16x32_bf16 v[56:59], v[120:123], v[174:177], v[56:59]
	v_mfma_f32_16x16x32_bf16 v[44:47], v[108:111], v[182:185], v[44:47]
	v_mfma_f32_16x16x32_bf16 v[40:43], v[120:123], v[182:185], v[40:43]
	v_mfma_f32_16x16x32_bf16 v[28:31], v[108:111], v[190:193], v[28:31]
	v_mfma_f32_16x16x32_bf16 v[24:27], v[120:123], v[190:193], v[24:27]
	v_mfma_f32_16x16x32_bf16 v[12:15], v[108:111], v[198:201], v[12:15]
	v_mfma_f32_16x16x32_bf16 v[8:11], v[120:123], v[198:201], v[8:11]
	v_mfma_f32_16x16x32_bf16 v[60:63], v[112:115], v[178:181], v[60:63]
	v_mfma_f32_16x16x32_bf16 v[56:59], v[124:127], v[178:181], v[56:59]
	v_mfma_f32_16x16x32_bf16 v[44:47], v[112:115], v[186:189], v[44:47]
	v_mfma_f32_16x16x32_bf16 v[40:43], v[124:127], v[186:189], v[40:43]
	v_mfma_f32_16x16x32_bf16 v[28:31], v[112:115], v[194:197], v[28:31]
	v_mfma_f32_16x16x32_bf16 v[24:27], v[124:127], v[194:197], v[24:27]
	v_mfma_f32_16x16x32_bf16 v[12:15], v[112:115], v[202:205], v[12:15]
	v_mfma_f32_16x16x32_bf16 v[8:11], v[124:127], v[202:205], v[8:11]
	s_setprio 0
	s_setprio 1
	v_mfma_f32_16x16x32_bf16 v[52:55], v[158:161], v[174:177], v[52:55]
	v_mfma_f32_16x16x32_bf16 v[48:51], v[166:169], v[174:177], v[48:51]
	v_mfma_f32_16x16x32_bf16 v[36:39], v[158:161], v[182:185], v[36:39]
	v_mfma_f32_16x16x32_bf16 v[32:35], v[166:169], v[182:185], v[32:35]
	v_mfma_f32_16x16x32_bf16 v[20:23], v[158:161], v[190:193], v[20:23]
	v_mfma_f32_16x16x32_bf16 v[16:19], v[166:169], v[190:193], v[16:19]
	v_mfma_f32_16x16x32_bf16 v[4:7], v[158:161], v[198:201], v[4:7]
	v_mfma_f32_16x16x32_bf16 v[0:3], v[166:169], v[198:201], v[0:3]
	v_mfma_f32_16x16x32_bf16 v[52:55], v[162:165], v[178:181], v[52:55]
	v_mfma_f32_16x16x32_bf16 v[48:51], v[170:173], v[178:181], v[48:51]
	v_mfma_f32_16x16x32_bf16 v[36:39], v[162:165], v[186:189], v[36:39]
	v_mfma_f32_16x16x32_bf16 v[32:35], v[170:173], v[186:189], v[32:35]
	v_mfma_f32_16x16x32_bf16 v[20:23], v[162:165], v[194:197], v[20:23]
	v_mfma_f32_16x16x32_bf16 v[16:19], v[170:173], v[194:197], v[16:19]
	v_mfma_f32_16x16x32_bf16 v[4:7], v[162:165], v[202:205], v[4:7]
	v_mfma_f32_16x16x32_bf16 v[0:3], v[170:173], v[202:205], v[0:3]
	s_setprio 0
	s_barrier
	v_add_u32_e32 v124, s62, v156
	v_add_u32_e32 v170, s67, v156
	ds_read_b128 v[108:111], v124
	ds_read_b128 v[112:115], v124 offset:1024
	ds_read_b128 v[120:123], v124 offset:2048
	ds_read_b128 v[124:127], v124 offset:3072
	ds_read_b128 v[158:161], v170
	ds_read_b128 v[162:165], v170 offset:1024
	ds_read_b128 v[166:169], v170 offset:2048
	ds_read_b128 v[170:173], v170 offset:3072
	s_add_u32 s0, s52, 0x4000
	s_addc_u32 s1, s53, 0
	s_mov_b32 m0, s58
	v_lshl_add_u64 v[206:207], s[0:1], 0, v[144:145]
	ds_read_b128 v[174:177], v157 offset:32768
	ds_read_b128 v[178:181], v157 offset:33792
	ds_read_b128 v[182:185], v157 offset:34816
	ds_read_b128 v[186:189], v157 offset:35840
	ds_read_b128 v[190:193], v157 offset:36864
	ds_read_b128 v[194:197], v157 offset:37888
	ds_read_b128 v[198:201], v157 offset:38912
	ds_read_b128 v[202:205], v157 offset:39936
	global_load_lds_dwordx4 v[206:207], off
	v_lshl_add_u64 v[206:207], s[0:1], 0, v[148:149]
	s_mov_b32 m0, s59
	s_nop 0
	global_load_lds_dwordx4 v[206:207], off
	s_waitcnt vmcnt(8)
	s_waitcnt lgkmcnt(0)
	s_barrier
	s_setprio 1
	s_waitcnt lgkmcnt(0)
	v_mfma_f32_16x16x32_bf16 v[140:143], v[108:111], v[174:177], v[140:143]
	v_mfma_f32_16x16x32_bf16 v[136:139], v[120:123], v[174:177], v[136:139]
	v_mfma_f32_16x16x32_bf16 v[116:119], v[108:111], v[182:185], v[116:119]
	v_mfma_f32_16x16x32_bf16 v[104:107], v[120:123], v[182:185], v[104:107]
	v_mfma_f32_16x16x32_bf16 v[92:95], v[108:111], v[190:193], v[92:95]
	v_mfma_f32_16x16x32_bf16 v[88:91], v[120:123], v[190:193], v[88:91]
	v_mfma_f32_16x16x32_bf16 v[76:79], v[108:111], v[198:201], v[76:79]
	v_mfma_f32_16x16x32_bf16 v[72:75], v[120:123], v[198:201], v[72:75]
	v_mfma_f32_16x16x32_bf16 v[140:143], v[112:115], v[178:181], v[140:143]
	v_mfma_f32_16x16x32_bf16 v[136:139], v[124:127], v[178:181], v[136:139]
	v_mfma_f32_16x16x32_bf16 v[116:119], v[112:115], v[186:189], v[116:119]
	v_mfma_f32_16x16x32_bf16 v[104:107], v[124:127], v[186:189], v[104:107]
	v_mfma_f32_16x16x32_bf16 v[92:95], v[112:115], v[194:197], v[92:95]
	v_mfma_f32_16x16x32_bf16 v[88:91], v[124:127], v[194:197], v[88:91]
	v_mfma_f32_16x16x32_bf16 v[76:79], v[112:115], v[202:205], v[76:79]
	v_mfma_f32_16x16x32_bf16 v[72:75], v[124:127], v[202:205], v[72:75]
	s_setprio 0
	s_setprio 1
	v_mfma_f32_16x16x32_bf16 v[132:135], v[158:161], v[174:177], v[132:135]
	v_mfma_f32_16x16x32_bf16 v[128:131], v[166:169], v[174:177], v[128:131]
	v_mfma_f32_16x16x32_bf16 v[100:103], v[158:161], v[182:185], v[100:103]
	v_mfma_f32_16x16x32_bf16 v[96:99], v[166:169], v[182:185], v[96:99]
	v_mfma_f32_16x16x32_bf16 v[84:87], v[158:161], v[190:193], v[84:87]
	v_mfma_f32_16x16x32_bf16 v[80:83], v[166:169], v[190:193], v[80:83]
	v_mfma_f32_16x16x32_bf16 v[68:71], v[158:161], v[198:201], v[68:71]
	v_mfma_f32_16x16x32_bf16 v[64:67], v[166:169], v[198:201], v[64:67]
	v_mfma_f32_16x16x32_bf16 v[132:135], v[162:165], v[178:181], v[132:135]
	v_mfma_f32_16x16x32_bf16 v[128:131], v[170:173], v[178:181], v[128:131]
	v_mfma_f32_16x16x32_bf16 v[100:103], v[162:165], v[186:189], v[100:103]
	v_mfma_f32_16x16x32_bf16 v[96:99], v[170:173], v[186:189], v[96:99]
	v_mfma_f32_16x16x32_bf16 v[84:87], v[162:165], v[194:197], v[84:87]
	v_mfma_f32_16x16x32_bf16 v[80:83], v[170:173], v[194:197], v[80:83]
	v_mfma_f32_16x16x32_bf16 v[68:71], v[162:165], v[202:205], v[68:71]
	v_mfma_f32_16x16x32_bf16 v[64:67], v[170:173], v[202:205], v[64:67]
	s_setprio 0
	s_barrier
	s_add_u32 s0, s50, 0x8000
	s_addc_u32 s1, s51, 0
	s_mov_b32 m0, s63
	v_lshl_add_u64 v[206:207], s[0:1], 0, v[146:147]
	ds_read_b128 v[174:177], v157 offset:49152
	ds_read_b128 v[178:181], v157 offset:50176
	ds_read_b128 v[182:185], v157 offset:51200
	ds_read_b128 v[186:189], v157 offset:52224
	ds_read_b128 v[190:193], v157 offset:53248
	ds_read_b128 v[194:197], v157 offset:54272
	ds_read_b128 v[198:201], v157 offset:55296
	ds_read_b128 v[202:205], v157 offset:56320
	global_load_lds_dwordx4 v[206:207], off
	v_lshl_add_u64 v[206:207], s[0:1], 0, v[150:151]
	s_add_u32 s0, s50, 0xc000
	s_mov_b32 m0, s64
	s_addc_u32 s1, s51, 0
	global_load_lds_dwordx4 v[206:207], off
	v_lshl_add_u64 v[206:207], s[0:1], 0, v[146:147]
	s_mov_b32 m0, s68
	s_nop 0
	global_load_lds_dwordx4 v[206:207], off
	v_lshl_add_u64 v[206:207], s[0:1], 0, v[150:151]
	s_mov_b32 m0, s69
	s_nop 0
	global_load_lds_dwordx4 v[206:207], off
	v_lshl_add_u64 v[206:207], s[48:49], 0, v[144:145]
	s_mov_b32 m0, s65
	s_nop 0
	global_load_lds_dwordx4 v[206:207], off
	v_lshl_add_u64 v[206:207], s[48:49], 0, v[148:149]
	s_mov_b32 m0, s66
	s_nop 0
	global_load_lds_dwordx4 v[206:207], off
	s_waitcnt vmcnt(8)
	s_waitcnt lgkmcnt(0)
	s_barrier
	s_setprio 1
	s_waitcnt lgkmcnt(0)
	v_mfma_f32_16x16x32_bf16 v[60:63], v[108:111], v[174:177], v[60:63]
	v_mfma_f32_16x16x32_bf16 v[56:59], v[120:123], v[174:177], v[56:59]
	v_mfma_f32_16x16x32_bf16 v[44:47], v[108:111], v[182:185], v[44:47]
	v_mfma_f32_16x16x32_bf16 v[40:43], v[120:123], v[182:185], v[40:43]
	v_mfma_f32_16x16x32_bf16 v[28:31], v[108:111], v[190:193], v[28:31]
	v_mfma_f32_16x16x32_bf16 v[24:27], v[120:123], v[190:193], v[24:27]
	v_mfma_f32_16x16x32_bf16 v[12:15], v[108:111], v[198:201], v[12:15]
	v_mfma_f32_16x16x32_bf16 v[8:11], v[120:123], v[198:201], v[8:11]
	v_mfma_f32_16x16x32_bf16 v[60:63], v[112:115], v[178:181], v[60:63]
	v_mfma_f32_16x16x32_bf16 v[56:59], v[124:127], v[178:181], v[56:59]
	v_mfma_f32_16x16x32_bf16 v[44:47], v[112:115], v[186:189], v[44:47]
	v_mfma_f32_16x16x32_bf16 v[40:43], v[124:127], v[186:189], v[40:43]
	v_mfma_f32_16x16x32_bf16 v[28:31], v[112:115], v[194:197], v[28:31]
	v_mfma_f32_16x16x32_bf16 v[24:27], v[124:127], v[194:197], v[24:27]
	v_mfma_f32_16x16x32_bf16 v[12:15], v[112:115], v[202:205], v[12:15]
	v_mfma_f32_16x16x32_bf16 v[8:11], v[124:127], v[202:205], v[8:11]
	s_setprio 0
	s_setprio 1
	v_mfma_f32_16x16x32_bf16 v[52:55], v[158:161], v[174:177], v[52:55]
	v_mfma_f32_16x16x32_bf16 v[48:51], v[166:169], v[174:177], v[48:51]
	v_mfma_f32_16x16x32_bf16 v[36:39], v[158:161], v[182:185], v[36:39]
	v_mfma_f32_16x16x32_bf16 v[32:35], v[166:169], v[182:185], v[32:35]
	v_mfma_f32_16x16x32_bf16 v[20:23], v[158:161], v[190:193], v[20:23]
	v_mfma_f32_16x16x32_bf16 v[16:19], v[166:169], v[190:193], v[16:19]
	v_mfma_f32_16x16x32_bf16 v[4:7], v[158:161], v[198:201], v[4:7]
	v_mfma_f32_16x16x32_bf16 v[0:3], v[166:169], v[198:201], v[0:3]
	v_mfma_f32_16x16x32_bf16 v[52:55], v[162:165], v[178:181], v[52:55]
	v_mfma_f32_16x16x32_bf16 v[48:51], v[170:173], v[178:181], v[48:51]
	v_mfma_f32_16x16x32_bf16 v[36:39], v[162:165], v[186:189], v[36:39]
	v_mfma_f32_16x16x32_bf16 v[32:35], v[170:173], v[186:189], v[32:35]
	v_mfma_f32_16x16x32_bf16 v[20:23], v[162:165], v[194:197], v[20:23]
	v_mfma_f32_16x16x32_bf16 v[16:19], v[170:173], v[194:197], v[16:19]
	v_mfma_f32_16x16x32_bf16 v[4:7], v[162:165], v[202:205], v[4:7]
	v_mfma_f32_16x16x32_bf16 v[0:3], v[170:173], v[202:205], v[0:3]
	s_setprio 0
	v_add_u32_e32 v124, s28, v156
	v_add_u32_e32 v170, s45, v156
	s_add_i32 s78, s78, 2
	s_add_u32 s76, s76, 0x10000
	s_addc_u32 s77, s77, 0
	s_mov_b64 s[0:1], s[46:47]
	s_cmp_gt_u32 s78, 29
	s_barrier
	s_cbranch_scc0 .LBB0_1173
	s_and_b64 vcc, exec, s[24:25]
	s_cbranch_vccz .LBB0_1176
	s_barrier

.LBB0_1247:
	s_ashr_i32 s35, s34, 31
	s_lshl_b64 s[4:5], s[34:35], 22
	s_add_u32 s38, s17, s4
	s_addc_u32 s39, s18, s5
	s_and_b64 s[4:5], s[36:37], exec
	s_cselect_b32 s4, s39, s1
	s_cselect_b32 s5, s38, s0
	s_ashr_i32 s25, s24, 31
	s_lshl_b64 s[40:41], s[24:25], 22
	s_add_u32 s40, s19, s40
	s_addc_u32 s41, s28, s41
	s_and_b64 s[46:47], s[36:37], exec
	s_cselect_b32 s25, s41, s45
	s_cselect_b32 s35, s40, s44
	s_add_u32 s74, s44, 0x10000
	s_addc_u32 s75, s45, 0
	s_mov_b32 s76, -2
	v_add_u32_e32 v92, s30, v206
	v_add_u32_e32 v156, s52, v206
	ds_read_b128 v[72:75], v92
	ds_read_b128 v[76:79], v92 offset:1024
	ds_read_b128 v[84:87], v92 offset:2048
	ds_read_b128 v[92:95], v92 offset:3072
	ds_read_b128 v[144:147], v156
	ds_read_b128 v[148:151], v156 offset:1024
	ds_read_b128 v[152:155], v156 offset:2048
	ds_read_b128 v[156:159], v156 offset:3072
	s_add_u32 s44, s0, 0x10000
	s_addc_u32 s45, s1, 0
	s_cmpk_eq_i32 s76, 0x7c
	s_cselect_b32 s50, s5, s44
	s_cselect_b32 s51, s4, s45
	s_cselect_b32 s48, s35, s74
	s_cselect_b32 s49, s25, s75
	s_add_u32 s46, s50, 0x8000
	s_addc_u32 s47, s51, 0
	v_lshl_add_u64 v[204:205], s[0:1], 0, v[180:181]
	s_add_i32 m0, s56, 0xc000
	ds_read_b128 v[160:163], v207
	ds_read_b128 v[164:167], v207 offset:1024
	ds_read_b128 v[168:171], v207 offset:2048
	ds_read_b128 v[184:187], v207 offset:3072
	ds_read_b128 v[188:191], v207 offset:4096
	ds_read_b128 v[192:195], v207 offset:5120
	ds_read_b128 v[196:199], v207 offset:6144
	ds_read_b128 v[200:203], v207 offset:7168
	global_load_lds_dwordx4 v[204:205], off
	v_lshl_add_u64 v[204:205], s[0:1], 0, v[182:183]
	s_add_i32 m0, s56, 0xe000
	s_nop 0
	global_load_lds_dwordx4 v[204:205], off
	s_waitcnt vmcnt(8)
	s_waitcnt lgkmcnt(0)
	s_barrier
	s_setprio 1
	s_waitcnt lgkmcnt(0)
	v_mfma_f32_16x16x32_bf16 v[140:143], v[72:75], v[160:163], 0
	v_mfma_f32_16x16x32_bf16 v[136:139], v[84:87], v[160:163], 0
	v_mfma_f32_16x16x32_bf16 v[124:127], v[72:75], v[168:171], 0
	v_mfma_f32_16x16x32_bf16 v[120:123], v[84:87], v[168:171], 0
	v_mfma_f32_16x16x32_bf16 v[108:111], v[72:75], v[188:191], 0
	v_mfma_f32_16x16x32_bf16 v[104:107], v[84:87], v[188:191], 0
	v_mfma_f32_16x16x32_bf16 v[88:91], v[72:75], v[196:199], 0
	v_mfma_f32_16x16x32_bf16 v[80:83], v[84:87], v[196:199], 0
	v_mfma_f32_16x16x32_bf16 v[140:143], v[76:79], v[164:167], v[140:143]
	v_mfma_f32_16x16x32_bf16 v[136:139], v[92:95], v[164:167], v[136:139]
	v_mfma_f32_16x16x32_bf16 v[124:127], v[76:79], v[184:187], v[124:127]
	v_mfma_f32_16x16x32_bf16 v[120:123], v[92:95], v[184:187], v[120:123]
	v_mfma_f32_16x16x32_bf16 v[108:111], v[76:79], v[192:195], v[108:111]
	v_mfma_f32_16x16x32_bf16 v[104:107], v[92:95], v[192:195], v[104:107]
	v_mfma_f32_16x16x32_bf16 v[88:91], v[76:79], v[200:203], v[88:91]
	v_mfma_f32_16x16x32_bf16 v[80:83], v[92:95], v[200:203], v[80:83]
	s_setprio 0
	s_setprio 1
	v_mfma_f32_16x16x32_bf16 v[132:135], v[144:147], v[160:163], 0
	v_mfma_f32_16x16x32_bf16 v[128:131], v[152:155], v[160:163], 0
	v_mfma_f32_16x16x32_bf16 v[116:119], v[144:147], v[168:171], 0
	v_mfma_f32_16x16x32_bf16 v[112:115], v[152:155], v[168:171], 0
	v_mfma_f32_16x16x32_bf16 v[100:103], v[144:147], v[188:191], 0
	v_mfma_f32_16x16x32_bf16 v[96:99], v[152:155], v[188:191], 0
	v_mfma_f32_16x16x32_bf16 v[68:71], v[144:147], v[196:199], 0
	v_mfma_f32_16x16x32_bf16 v[64:67], v[152:155], v[196:199], 0
	v_mfma_f32_16x16x32_bf16 v[132:135], v[148:151], v[164:167], v[132:135]
	v_mfma_f32_16x16x32_bf16 v[128:131], v[156:159], v[164:167], v[128:131]
	v_mfma_f32_16x16x32_bf16 v[116:119], v[148:151], v[184:187], v[116:119]
	v_mfma_f32_16x16x32_bf16 v[112:115], v[156:159], v[184:187], v[112:115]
	v_mfma_f32_16x16x32_bf16 v[100:103], v[148:151], v[192:195], v[100:103]
	v_mfma_f32_16x16x32_bf16 v[96:99], v[156:159], v[192:195], v[96:99]
	v_mfma_f32_16x16x32_bf16 v[68:71], v[148:151], v[200:203], v[68:71]
	v_mfma_f32_16x16x32_bf16 v[64:67], v[156:159], v[200:203], v[64:67]
	s_setprio 0
	s_barrier
	s_mov_b32 m0, s31
	v_lshl_add_u64 v[204:205], s[48:49], 0, v[174:175]
	s_add_u32 s0, s48, 0x4000
	ds_read_b128 v[160:163], v207 offset:16384
	ds_read_b128 v[164:167], v207 offset:17408
	ds_read_b128 v[168:171], v207 offset:18432
	ds_read_b128 v[184:187], v207 offset:19456
	ds_read_b128 v[188:191], v207 offset:20480
	ds_read_b128 v[192:195], v207 offset:21504
	ds_read_b128 v[196:199], v207 offset:22528
	ds_read_b128 v[200:203], v207 offset:23552
	global_load_lds_dwordx4 v[204:205], off
	v_lshl_add_u64 v[204:205], s[48:49], 0, v[178:179]
	s_mov_b32 m0, s43
	s_addc_u32 s1, s49, 0
	global_load_lds_dwordx4 v[204:205], off
	v_lshl_add_u64 v[204:205], s[0:1], 0, v[174:175]
	s_mov_b32 m0, s53
	s_nop 0
	global_load_lds_dwordx4 v[204:205], off
	v_lshl_add_u64 v[204:205], s[0:1], 0, v[178:179]
	s_mov_b32 m0, s54
	s_nop 0
	global_load_lds_dwordx4 v[204:205], off
	v_lshl_add_u64 v[204:205], s[50:51], 0, v[172:173]
	s_mov_b32 m0, s56
	s_nop 0
	global_load_lds_dwordx4 v[204:205], off
	v_lshl_add_u64 v[204:205], s[50:51], 0, v[176:177]
	s_mov_b32 m0, s57
	s_nop 0
	global_load_lds_dwordx4 v[204:205], off
	s_waitcnt vmcnt(8)
	s_waitcnt lgkmcnt(0)
	s_barrier
	s_setprio 1
	s_waitcnt lgkmcnt(0)
	v_mfma_f32_16x16x32_bf16 v[60:63], v[72:75], v[160:163], 0
	v_mfma_f32_16x16x32_bf16 v[56:59], v[84:87], v[160:163], 0
	v_mfma_f32_16x16x32_bf16 v[44:47], v[72:75], v[168:171], 0
	v_mfma_f32_16x16x32_bf16 v[40:43], v[84:87], v[168:171], 0
	v_mfma_f32_16x16x32_bf16 v[28:31], v[72:75], v[188:191], 0
	v_mfma_f32_16x16x32_bf16 v[24:27], v[84:87], v[188:191], 0
	v_mfma_f32_16x16x32_bf16 v[12:15], v[72:75], v[196:199], 0
	v_mfma_f32_16x16x32_bf16 v[8:11], v[84:87], v[196:199], 0
	v_mfma_f32_16x16x32_bf16 v[60:63], v[76:79], v[164:167], v[60:63]
	v_mfma_f32_16x16x32_bf16 v[56:59], v[92:95], v[164:167], v[56:59]
	v_mfma_f32_16x16x32_bf16 v[44:47], v[76:79], v[184:187], v[44:47]
	v_mfma_f32_16x16x32_bf16 v[40:43], v[92:95], v[184:187], v[40:43]
	v_mfma_f32_16x16x32_bf16 v[28:31], v[76:79], v[192:195], v[28:31]
	v_mfma_f32_16x16x32_bf16 v[24:27], v[92:95], v[192:195], v[24:27]
	v_mfma_f32_16x16x32_bf16 v[12:15], v[76:79], v[200:203], v[12:15]
	v_mfma_f32_16x16x32_bf16 v[8:11], v[92:95], v[200:203], v[8:11]
	s_setprio 0
	s_setprio 1
	v_mfma_f32_16x16x32_bf16 v[52:55], v[144:147], v[160:163], 0
	v_mfma_f32_16x16x32_bf16 v[48:51], v[152:155], v[160:163], 0
	v_mfma_f32_16x16x32_bf16 v[36:39], v[144:147], v[168:171], 0
	v_mfma_f32_16x16x32_bf16 v[32:35], v[152:155], v[168:171], 0
	v_mfma_f32_16x16x32_bf16 v[20:23], v[144:147], v[188:191], 0
	v_mfma_f32_16x16x32_bf16 v[16:19], v[152:155], v[188:191], 0
	v_mfma_f32_16x16x32_bf16 v[4:7], v[144:147], v[196:199], 0
	v_mfma_f32_16x16x32_bf16 v[0:3], v[152:155], v[196:199], 0
	v_mfma_f32_16x16x32_bf16 v[52:55], v[148:151], v[164:167], v[52:55]
	v_mfma_f32_16x16x32_bf16 v[48:51], v[156:159], v[164:167], v[48:51]
	v_mfma_f32_16x16x32_bf16 v[36:39], v[148:151], v[184:187], v[36:39]
	v_mfma_f32_16x16x32_bf16 v[32:35], v[156:159], v[184:187], v[32:35]
	v_mfma_f32_16x16x32_bf16 v[20:23], v[148:151], v[192:195], v[20:23]
	v_mfma_f32_16x16x32_bf16 v[16:19], v[156:159], v[192:195], v[16:19]
	v_mfma_f32_16x16x32_bf16 v[4:7], v[148:151], v[200:203], v[4:7]
	v_mfma_f32_16x16x32_bf16 v[0:3], v[156:159], v[200:203], v[0:3]
	s_setprio 0
	s_barrier
	v_add_u32_e32 v92, s64, v206
	v_add_u32_e32 v156, s69, v206
	ds_read_b128 v[72:75], v92
	ds_read_b128 v[76:79], v92 offset:1024
	ds_read_b128 v[84:87], v92 offset:2048
	ds_read_b128 v[92:95], v92 offset:3072
	ds_read_b128 v[144:147], v156
	ds_read_b128 v[148:151], v156 offset:1024
	ds_read_b128 v[152:155], v156 offset:2048
	ds_read_b128 v[156:159], v156 offset:3072
	s_add_u32 s0, s50, 0x4000
	s_addc_u32 s1, s51, 0
	s_mov_b32 m0, s58
	v_lshl_add_u64 v[204:205], s[0:1], 0, v[172:173]
	ds_read_b128 v[160:163], v207 offset:32768
	ds_read_b128 v[164:167], v207 offset:33792
	ds_read_b128 v[168:171], v207 offset:34816
	ds_read_b128 v[184:187], v207 offset:35840
	ds_read_b128 v[188:191], v207 offset:36864
	ds_read_b128 v[192:195], v207 offset:37888
	ds_read_b128 v[196:199], v207 offset:38912
	ds_read_b128 v[200:203], v207 offset:39936
	global_load_lds_dwordx4 v[204:205], off
	v_lshl_add_u64 v[204:205], s[0:1], 0, v[176:177]
	s_mov_b32 m0, s59
	s_nop 0
	global_load_lds_dwordx4 v[204:205], off
	s_waitcnt vmcnt(8)
	s_waitcnt lgkmcnt(0)
	s_barrier
	s_setprio 1
	s_waitcnt lgkmcnt(0)
	v_mfma_f32_16x16x32_bf16 v[140:143], v[72:75], v[160:163], v[140:143]
	v_mfma_f32_16x16x32_bf16 v[136:139], v[84:87], v[160:163], v[136:139]
	v_mfma_f32_16x16x32_bf16 v[124:127], v[72:75], v[168:171], v[124:127]
	v_mfma_f32_16x16x32_bf16 v[120:123], v[84:87], v[168:171], v[120:123]
	v_mfma_f32_16x16x32_bf16 v[108:111], v[72:75], v[188:191], v[108:111]
	v_mfma_f32_16x16x32_bf16 v[104:107], v[84:87], v[188:191], v[104:107]
	v_mfma_f32_16x16x32_bf16 v[88:91], v[72:75], v[196:199], v[88:91]
	v_mfma_f32_16x16x32_bf16 v[80:83], v[84:87], v[196:199], v[80:83]
	v_mfma_f32_16x16x32_bf16 v[140:143], v[76:79], v[164:167], v[140:143]
	v_mfma_f32_16x16x32_bf16 v[136:139], v[92:95], v[164:167], v[136:139]
	v_mfma_f32_16x16x32_bf16 v[124:127], v[76:79], v[184:187], v[124:127]
	v_mfma_f32_16x16x32_bf16 v[120:123], v[92:95], v[184:187], v[120:123]
	v_mfma_f32_16x16x32_bf16 v[108:111], v[76:79], v[192:195], v[108:111]
	v_mfma_f32_16x16x32_bf16 v[104:107], v[92:95], v[192:195], v[104:107]
	v_mfma_f32_16x16x32_bf16 v[88:91], v[76:79], v[200:203], v[88:91]
	v_mfma_f32_16x16x32_bf16 v[80:83], v[92:95], v[200:203], v[80:83]
	s_setprio 0
	s_setprio 1
	v_mfma_f32_16x16x32_bf16 v[132:135], v[144:147], v[160:163], v[132:135]
	v_mfma_f32_16x16x32_bf16 v[128:131], v[152:155], v[160:163], v[128:131]
	v_mfma_f32_16x16x32_bf16 v[116:119], v[144:147], v[168:171], v[116:119]
	v_mfma_f32_16x16x32_bf16 v[112:115], v[152:155], v[168:171], v[112:115]
	v_mfma_f32_16x16x32_bf16 v[100:103], v[144:147], v[188:191], v[100:103]
	v_mfma_f32_16x16x32_bf16 v[96:99], v[152:155], v[188:191], v[96:99]
	v_mfma_f32_16x16x32_bf16 v[68:71], v[144:147], v[196:199], v[68:71]
	v_mfma_f32_16x16x32_bf16 v[64:67], v[152:155], v[196:199], v[64:67]
	v_mfma_f32_16x16x32_bf16 v[132:135], v[148:151], v[164:167], v[132:135]
	v_mfma_f32_16x16x32_bf16 v[128:131], v[156:159], v[164:167], v[128:131]
	v_mfma_f32_16x16x32_bf16 v[116:119], v[148:151], v[184:187], v[116:119]
	v_mfma_f32_16x16x32_bf16 v[112:115], v[156:159], v[184:187], v[112:115]
	v_mfma_f32_16x16x32_bf16 v[100:103], v[148:151], v[192:195], v[100:103]
	v_mfma_f32_16x16x32_bf16 v[96:99], v[156:159], v[192:195], v[96:99]
	v_mfma_f32_16x16x32_bf16 v[68:71], v[148:151], v[200:203], v[68:71]
	v_mfma_f32_16x16x32_bf16 v[64:67], v[156:159], v[200:203], v[64:67]
	s_setprio 0
	s_barrier
	s_add_u32 s0, s48, 0x8000
	s_addc_u32 s1, s49, 0
	s_mov_b32 m0, s65
	v_lshl_add_u64 v[204:205], s[0:1], 0, v[174:175]
	ds_read_b128 v[160:163], v207 offset:49152
	ds_read_b128 v[164:167], v207 offset:50176
	ds_read_b128 v[168:171], v207 offset:51200
	ds_read_b128 v[184:187], v207 offset:52224
	ds_read_b128 v[188:191], v207 offset:53248
	ds_read_b128 v[192:195], v207 offset:54272
	ds_read_b128 v[196:199], v207 offset:55296
	ds_read_b128 v[200:203], v207 offset:56320
	global_load_lds_dwordx4 v[204:205], off
	v_lshl_add_u64 v[204:205], s[0:1], 0, v[178:179]
	s_add_u32 s0, s48, 0xc000
	s_mov_b32 m0, s66
	s_addc_u32 s1, s49, 0
	global_load_lds_dwordx4 v[204:205], off
	v_lshl_add_u64 v[204:205], s[0:1], 0, v[174:175]
	s_mov_b32 m0, s70
	s_nop 0
	global_load_lds_dwordx4 v[204:205], off
	v_lshl_add_u64 v[204:205], s[0:1], 0, v[178:179]
	s_mov_b32 m0, s71
	s_nop 0
	global_load_lds_dwordx4 v[204:205], off
	v_lshl_add_u64 v[204:205], s[46:47], 0, v[172:173]
	s_mov_b32 m0, s67
	s_nop 0
	global_load_lds_dwordx4 v[204:205], off
	v_lshl_add_u64 v[204:205], s[46:47], 0, v[176:177]
	s_mov_b32 m0, s68
	s_nop 0
	global_load_lds_dwordx4 v[204:205], off
	s_waitcnt vmcnt(8)
	s_waitcnt lgkmcnt(0)
	s_barrier
	s_setprio 1
	s_waitcnt lgkmcnt(0)
	v_mfma_f32_16x16x32_bf16 v[60:63], v[72:75], v[160:163], v[60:63]
	v_mfma_f32_16x16x32_bf16 v[56:59], v[84:87], v[160:163], v[56:59]
	v_mfma_f32_16x16x32_bf16 v[44:47], v[72:75], v[168:171], v[44:47]
	v_mfma_f32_16x16x32_bf16 v[40:43], v[84:87], v[168:171], v[40:43]
	v_mfma_f32_16x16x32_bf16 v[28:31], v[72:75], v[188:191], v[28:31]
	v_mfma_f32_16x16x32_bf16 v[24:27], v[84:87], v[188:191], v[24:27]
	v_mfma_f32_16x16x32_bf16 v[12:15], v[72:75], v[196:199], v[12:15]
	v_mfma_f32_16x16x32_bf16 v[8:11], v[84:87], v[196:199], v[8:11]
	v_mfma_f32_16x16x32_bf16 v[60:63], v[76:79], v[164:167], v[60:63]
	v_mfma_f32_16x16x32_bf16 v[56:59], v[92:95], v[164:167], v[56:59]
	v_mfma_f32_16x16x32_bf16 v[44:47], v[76:79], v[184:187], v[44:47]
	v_mfma_f32_16x16x32_bf16 v[40:43], v[92:95], v[184:187], v[40:43]
	v_mfma_f32_16x16x32_bf16 v[28:31], v[76:79], v[192:195], v[28:31]
	v_mfma_f32_16x16x32_bf16 v[24:27], v[92:95], v[192:195], v[24:27]
	v_mfma_f32_16x16x32_bf16 v[12:15], v[76:79], v[200:203], v[12:15]
	v_mfma_f32_16x16x32_bf16 v[8:11], v[92:95], v[200:203], v[8:11]
	s_setprio 0
	s_setprio 1
	v_mfma_f32_16x16x32_bf16 v[52:55], v[144:147], v[160:163], v[52:55]
	v_mfma_f32_16x16x32_bf16 v[48:51], v[152:155], v[160:163], v[48:51]
	v_mfma_f32_16x16x32_bf16 v[36:39], v[144:147], v[168:171], v[36:39]
	v_mfma_f32_16x16x32_bf16 v[32:35], v[152:155], v[168:171], v[32:35]
	v_mfma_f32_16x16x32_bf16 v[20:23], v[144:147], v[188:191], v[20:23]
	v_mfma_f32_16x16x32_bf16 v[16:19], v[152:155], v[188:191], v[16:19]
	v_mfma_f32_16x16x32_bf16 v[4:7], v[144:147], v[196:199], v[4:7]
	v_mfma_f32_16x16x32_bf16 v[0:3], v[152:155], v[196:199], v[0:3]
	v_mfma_f32_16x16x32_bf16 v[52:55], v[148:151], v[164:167], v[52:55]
	v_mfma_f32_16x16x32_bf16 v[48:51], v[156:159], v[164:167], v[48:51]
	v_mfma_f32_16x16x32_bf16 v[36:39], v[148:151], v[184:187], v[36:39]
	v_mfma_f32_16x16x32_bf16 v[32:35], v[156:159], v[184:187], v[32:35]
	v_mfma_f32_16x16x32_bf16 v[20:23], v[148:151], v[192:195], v[20:23]
	v_mfma_f32_16x16x32_bf16 v[16:19], v[156:159], v[192:195], v[16:19]
	v_mfma_f32_16x16x32_bf16 v[4:7], v[148:151], v[200:203], v[4:7]
	v_mfma_f32_16x16x32_bf16 v[0:3], v[156:159], v[200:203], v[0:3]
	s_setprio 0
	v_add_u32_e32 v92, s30, v206
	v_add_u32_e32 v156, s52, v206
	s_add_i32 s76, s76, 2
	s_add_u32 s74, s74, 0x10000
	s_addc_u32 s75, s75, 0
	s_mov_b64 s[0:1], s[44:45]
	s_cmpk_gt_u32 s76, 0x7d
	s_barrier
.LBB0_1248:
	ds_read_b128 v[72:75], v92
	ds_read_b128 v[76:79], v92 offset:1024
	ds_read_b128 v[84:87], v92 offset:2048
	ds_read_b128 v[92:95], v92 offset:3072
	ds_read_b128 v[144:147], v156
	ds_read_b128 v[148:151], v156 offset:1024
	ds_read_b128 v[152:155], v156 offset:2048
	ds_read_b128 v[156:159], v156 offset:3072
	s_add_u32 s44, s0, 0x10000
	s_addc_u32 s45, s1, 0
	s_cmpk_eq_i32 s76, 0x7c
	s_cselect_b32 s50, s5, s44
	s_cselect_b32 s51, s4, s45
	s_cselect_b32 s48, s35, s74
	s_cselect_b32 s49, s25, s75
	s_add_u32 s46, s50, 0x8000
	s_addc_u32 s47, s51, 0
	v_lshl_add_u64 v[204:205], s[0:1], 0, v[180:181]
	s_add_i32 m0, s56, 0xc000
	ds_read_b128 v[160:163], v207
	ds_read_b128 v[164:167], v207 offset:1024
	ds_read_b128 v[168:171], v207 offset:2048
	ds_read_b128 v[184:187], v207 offset:3072
	ds_read_b128 v[188:191], v207 offset:4096
	ds_read_b128 v[192:195], v207 offset:5120
	ds_read_b128 v[196:199], v207 offset:6144
	ds_read_b128 v[200:203], v207 offset:7168
	global_load_lds_dwordx4 v[204:205], off
	v_lshl_add_u64 v[204:205], s[0:1], 0, v[182:183]
	s_add_i32 m0, s56, 0xe000
	s_nop 0
	global_load_lds_dwordx4 v[204:205], off
	s_waitcnt vmcnt(8)
	s_waitcnt lgkmcnt(0)
	s_barrier
	s_setprio 1
	s_waitcnt lgkmcnt(0)
	v_mfma_f32_16x16x32_bf16 v[140:143], v[72:75], v[160:163], v[140:143]
	v_mfma_f32_16x16x32_bf16 v[136:139], v[84:87], v[160:163], v[136:139]
	v_mfma_f32_16x16x32_bf16 v[124:127], v[72:75], v[168:171], v[124:127]
	v_mfma_f32_16x16x32_bf16 v[120:123], v[84:87], v[168:171], v[120:123]
	v_mfma_f32_16x16x32_bf16 v[108:111], v[72:75], v[188:191], v[108:111]
	v_mfma_f32_16x16x32_bf16 v[104:107], v[84:87], v[188:191], v[104:107]
	v_mfma_f32_16x16x32_bf16 v[88:91], v[72:75], v[196:199], v[88:91]
	v_mfma_f32_16x16x32_bf16 v[80:83], v[84:87], v[196:199], v[80:83]
	v_mfma_f32_16x16x32_bf16 v[140:143], v[76:79], v[164:167], v[140:143]
	v_mfma_f32_16x16x32_bf16 v[136:139], v[92:95], v[164:167], v[136:139]
	v_mfma_f32_16x16x32_bf16 v[124:127], v[76:79], v[184:187], v[124:127]
	v_mfma_f32_16x16x32_bf16 v[120:123], v[92:95], v[184:187], v[120:123]
	v_mfma_f32_16x16x32_bf16 v[108:111], v[76:79], v[192:195], v[108:111]
	v_mfma_f32_16x16x32_bf16 v[104:107], v[92:95], v[192:195], v[104:107]
	v_mfma_f32_16x16x32_bf16 v[88:91], v[76:79], v[200:203], v[88:91]
	v_mfma_f32_16x16x32_bf16 v[80:83], v[92:95], v[200:203], v[80:83]
	s_setprio 0
	s_setprio 1
	v_mfma_f32_16x16x32_bf16 v[132:135], v[144:147], v[160:163], v[132:135]
	v_mfma_f32_16x16x32_bf16 v[128:131], v[152:155], v[160:163], v[128:131]
	v_mfma_f32_16x16x32_bf16 v[116:119], v[144:147], v[168:171], v[116:119]
	v_mfma_f32_16x16x32_bf16 v[112:115], v[152:155], v[168:171], v[112:115]
	v_mfma_f32_16x16x32_bf16 v[100:103], v[144:147], v[188:191], v[100:103]
	v_mfma_f32_16x16x32_bf16 v[96:99], v[152:155], v[188:191], v[96:99]
	v_mfma_f32_16x16x32_bf16 v[68:71], v[144:147], v[196:199], v[68:71]
	v_mfma_f32_16x16x32_bf16 v[64:67], v[152:155], v[196:199], v[64:67]
	v_mfma_f32_16x16x32_bf16 v[132:135], v[148:151], v[164:167], v[132:135]
	v_mfma_f32_16x16x32_bf16 v[128:131], v[156:159], v[164:167], v[128:131]
	v_mfma_f32_16x16x32_bf16 v[116:119], v[148:151], v[184:187], v[116:119]
	v_mfma_f32_16x16x32_bf16 v[112:115], v[156:159], v[184:187], v[112:115]
	v_mfma_f32_16x16x32_bf16 v[100:103], v[148:151], v[192:195], v[100:103]
	v_mfma_f32_16x16x32_bf16 v[96:99], v[156:159], v[192:195], v[96:99]
	v_mfma_f32_16x16x32_bf16 v[68:71], v[148:151], v[200:203], v[68:71]
	v_mfma_f32_16x16x32_bf16 v[64:67], v[156:159], v[200:203], v[64:67]
	s_setprio 0
	s_barrier
	s_mov_b32 m0, s31
	v_lshl_add_u64 v[204:205], s[48:49], 0, v[174:175]
	s_add_u32 s0, s48, 0x4000
	ds_read_b128 v[160:163], v207 offset:16384
	ds_read_b128 v[164:167], v207 offset:17408
	ds_read_b128 v[168:171], v207 offset:18432
	ds_read_b128 v[184:187], v207 offset:19456
	ds_read_b128 v[188:191], v207 offset:20480
	ds_read_b128 v[192:195], v207 offset:21504
	ds_read_b128 v[196:199], v207 offset:22528
	ds_read_b128 v[200:203], v207 offset:23552
	global_load_lds_dwordx4 v[204:205], off
	v_lshl_add_u64 v[204:205], s[48:49], 0, v[178:179]
	s_mov_b32 m0, s43
	s_addc_u32 s1, s49, 0
	global_load_lds_dwordx4 v[204:205], off
	v_lshl_add_u64 v[204:205], s[0:1], 0, v[174:175]
	s_mov_b32 m0, s53
	s_nop 0
	global_load_lds_dwordx4 v[204:205], off
	v_lshl_add_u64 v[204:205], s[0:1], 0, v[178:179]
	s_mov_b32 m0, s54
	s_nop 0
	global_load_lds_dwordx4 v[204:205], off
	v_lshl_add_u64 v[204:205], s[50:51], 0, v[172:173]
	s_mov_b32 m0, s56
	s_nop 0
	global_load_lds_dwordx4 v[204:205], off
	v_lshl_add_u64 v[204:205], s[50:51], 0, v[176:177]
	s_mov_b32 m0, s57
	s_nop 0
	global_load_lds_dwordx4 v[204:205], off
	s_waitcnt vmcnt(8)
	s_waitcnt lgkmcnt(0)
	s_barrier
	s_setprio 1
	s_waitcnt lgkmcnt(0)
	v_mfma_f32_16x16x32_bf16 v[60:63], v[72:75], v[160:163], v[60:63]
	v_mfma_f32_16x16x32_bf16 v[56:59], v[84:87], v[160:163], v[56:59]
	v_mfma_f32_16x16x32_bf16 v[44:47], v[72:75], v[168:171], v[44:47]
	v_mfma_f32_16x16x32_bf16 v[40:43], v[84:87], v[168:171], v[40:43]
	v_mfma_f32_16x16x32_bf16 v[28:31], v[72:75], v[188:191], v[28:31]
	v_mfma_f32_16x16x32_bf16 v[24:27], v[84:87], v[188:191], v[24:27]
	v_mfma_f32_16x16x32_bf16 v[12:15], v[72:75], v[196:199], v[12:15]
	v_mfma_f32_16x16x32_bf16 v[8:11], v[84:87], v[196:199], v[8:11]
	v_mfma_f32_16x16x32_bf16 v[60:63], v[76:79], v[164:167], v[60:63]
	v_mfma_f32_16x16x32_bf16 v[56:59], v[92:95], v[164:167], v[56:59]
	v_mfma_f32_16x16x32_bf16 v[44:47], v[76:79], v[184:187], v[44:47]
	v_mfma_f32_16x16x32_bf16 v[40:43], v[92:95], v[184:187], v[40:43]
	v_mfma_f32_16x16x32_bf16 v[28:31], v[76:79], v[192:195], v[28:31]
	v_mfma_f32_16x16x32_bf16 v[24:27], v[92:95], v[192:195], v[24:27]
	v_mfma_f32_16x16x32_bf16 v[12:15], v[76:79], v[200:203], v[12:15]
	v_mfma_f32_16x16x32_bf16 v[8:11], v[92:95], v[200:203], v[8:11]
	s_setprio 0
	s_setprio 1
	v_mfma_f32_16x16x32_bf16 v[52:55], v[144:147], v[160:163], v[52:55]
	v_mfma_f32_16x16x32_bf16 v[48:51], v[152:155], v[160:163], v[48:51]
	v_mfma_f32_16x16x32_bf16 v[36:39], v[144:147], v[168:171], v[36:39]
	v_mfma_f32_16x16x32_bf16 v[32:35], v[152:155], v[168:171], v[32:35]
	v_mfma_f32_16x16x32_bf16 v[20:23], v[144:147], v[188:191], v[20:23]
	v_mfma_f32_16x16x32_bf16 v[16:19], v[152:155], v[188:191], v[16:19]
	v_mfma_f32_16x16x32_bf16 v[4:7], v[144:147], v[196:199], v[4:7]
	v_mfma_f32_16x16x32_bf16 v[0:3], v[152:155], v[196:199], v[0:3]
	v_mfma_f32_16x16x32_bf16 v[52:55], v[148:151], v[164:167], v[52:55]
	v_mfma_f32_16x16x32_bf16 v[48:51], v[156:159], v[164:167], v[48:51]
	v_mfma_f32_16x16x32_bf16 v[36:39], v[148:151], v[184:187], v[36:39]
	v_mfma_f32_16x16x32_bf16 v[32:35], v[156:159], v[184:187], v[32:35]
	v_mfma_f32_16x16x32_bf16 v[20:23], v[148:151], v[192:195], v[20:23]
	v_mfma_f32_16x16x32_bf16 v[16:19], v[156:159], v[192:195], v[16:19]
	v_mfma_f32_16x16x32_bf16 v[4:7], v[148:151], v[200:203], v[4:7]
	v_mfma_f32_16x16x32_bf16 v[0:3], v[156:159], v[200:203], v[0:3]
	s_setprio 0
	s_barrier
	v_add_u32_e32 v92, s64, v206
	v_add_u32_e32 v156, s69, v206
	ds_read_b128 v[72:75], v92
	ds_read_b128 v[76:79], v92 offset:1024
	ds_read_b128 v[84:87], v92 offset:2048
	ds_read_b128 v[92:95], v92 offset:3072
	ds_read_b128 v[144:147], v156
	ds_read_b128 v[148:151], v156 offset:1024
	ds_read_b128 v[152:155], v156 offset:2048
	ds_read_b128 v[156:159], v156 offset:3072
	s_add_u32 s0, s50, 0x4000
	s_addc_u32 s1, s51, 0
	s_mov_b32 m0, s58
	v_lshl_add_u64 v[204:205], s[0:1], 0, v[172:173]
	ds_read_b128 v[160:163], v207 offset:32768
	ds_read_b128 v[164:167], v207 offset:33792
	ds_read_b128 v[168:171], v207 offset:34816
	ds_read_b128 v[184:187], v207 offset:35840
	ds_read_b128 v[188:191], v207 offset:36864
	ds_read_b128 v[192:195], v207 offset:37888
	ds_read_b128 v[196:199], v207 offset:38912
	ds_read_b128 v[200:203], v207 offset:39936
	global_load_lds_dwordx4 v[204:205], off
	v_lshl_add_u64 v[204:205], s[0:1], 0, v[176:177]
	s_mov_b32 m0, s59
	s_nop 0
	global_load_lds_dwordx4 v[204:205], off
	s_waitcnt vmcnt(8)
	s_waitcnt lgkmcnt(0)
	s_barrier
	s_setprio 1
	s_waitcnt lgkmcnt(0)
	v_mfma_f32_16x16x32_bf16 v[140:143], v[72:75], v[160:163], v[140:143]
	v_mfma_f32_16x16x32_bf16 v[136:139], v[84:87], v[160:163], v[136:139]
	v_mfma_f32_16x16x32_bf16 v[124:127], v[72:75], v[168:171], v[124:127]
	v_mfma_f32_16x16x32_bf16 v[120:123], v[84:87], v[168:171], v[120:123]
	v_mfma_f32_16x16x32_bf16 v[108:111], v[72:75], v[188:191], v[108:111]
	v_mfma_f32_16x16x32_bf16 v[104:107], v[84:87], v[188:191], v[104:107]
	v_mfma_f32_16x16x32_bf16 v[88:91], v[72:75], v[196:199], v[88:91]
	v_mfma_f32_16x16x32_bf16 v[80:83], v[84:87], v[196:199], v[80:83]
	v_mfma_f32_16x16x32_bf16 v[140:143], v[76:79], v[164:167], v[140:143]
	v_mfma_f32_16x16x32_bf16 v[136:139], v[92:95], v[164:167], v[136:139]
	v_mfma_f32_16x16x32_bf16 v[124:127], v[76:79], v[184:187], v[124:127]
	v_mfma_f32_16x16x32_bf16 v[120:123], v[92:95], v[184:187], v[120:123]
	v_mfma_f32_16x16x32_bf16 v[108:111], v[76:79], v[192:195], v[108:111]
	v_mfma_f32_16x16x32_bf16 v[104:107], v[92:95], v[192:195], v[104:107]
	v_mfma_f32_16x16x32_bf16 v[88:91], v[76:79], v[200:203], v[88:91]
	v_mfma_f32_16x16x32_bf16 v[80:83], v[92:95], v[200:203], v[80:83]
	s_setprio 0
	s_setprio 1
	v_mfma_f32_16x16x32_bf16 v[132:135], v[144:147], v[160:163], v[132:135]
	v_mfma_f32_16x16x32_bf16 v[128:131], v[152:155], v[160:163], v[128:131]
	v_mfma_f32_16x16x32_bf16 v[116:119], v[144:147], v[168:171], v[116:119]
	v_mfma_f32_16x16x32_bf16 v[112:115], v[152:155], v[168:171], v[112:115]
	v_mfma_f32_16x16x32_bf16 v[100:103], v[144:147], v[188:191], v[100:103]
	v_mfma_f32_16x16x32_bf16 v[96:99], v[152:155], v[188:191], v[96:99]
	v_mfma_f32_16x16x32_bf16 v[68:71], v[144:147], v[196:199], v[68:71]
	v_mfma_f32_16x16x32_bf16 v[64:67], v[152:155], v[196:199], v[64:67]
	v_mfma_f32_16x16x32_bf16 v[132:135], v[148:151], v[164:167], v[132:135]
	v_mfma_f32_16x16x32_bf16 v[128:131], v[156:159], v[164:167], v[128:131]
	v_mfma_f32_16x16x32_bf16 v[116:119], v[148:151], v[184:187], v[116:119]
	v_mfma_f32_16x16x32_bf16 v[112:115], v[156:159], v[184:187], v[112:115]
	v_mfma_f32_16x16x32_bf16 v[100:103], v[148:151], v[192:195], v[100:103]
	v_mfma_f32_16x16x32_bf16 v[96:99], v[156:159], v[192:195], v[96:99]
	v_mfma_f32_16x16x32_bf16 v[68:71], v[148:151], v[200:203], v[68:71]
	v_mfma_f32_16x16x32_bf16 v[64:67], v[156:159], v[200:203], v[64:67]
	s_setprio 0
	s_barrier
	s_add_u32 s0, s48, 0x8000
	s_addc_u32 s1, s49, 0
	s_mov_b32 m0, s65
	v_lshl_add_u64 v[204:205], s[0:1], 0, v[174:175]
	ds_read_b128 v[160:163], v207 offset:49152
	ds_read_b128 v[164:167], v207 offset:50176
	ds_read_b128 v[168:171], v207 offset:51200
	ds_read_b128 v[184:187], v207 offset:52224
	ds_read_b128 v[188:191], v207 offset:53248
	ds_read_b128 v[192:195], v207 offset:54272
	ds_read_b128 v[196:199], v207 offset:55296
	ds_read_b128 v[200:203], v207 offset:56320
	global_load_lds_dwordx4 v[204:205], off
	v_lshl_add_u64 v[204:205], s[0:1], 0, v[178:179]
	s_add_u32 s0, s48, 0xc000
	s_mov_b32 m0, s66
	s_addc_u32 s1, s49, 0
	global_load_lds_dwordx4 v[204:205], off
	v_lshl_add_u64 v[204:205], s[0:1], 0, v[174:175]
	s_mov_b32 m0, s70
	s_nop 0
	global_load_lds_dwordx4 v[204:205], off
	v_lshl_add_u64 v[204:205], s[0:1], 0, v[178:179]
	s_mov_b32 m0, s71
	s_nop 0
	global_load_lds_dwordx4 v[204:205], off
	v_lshl_add_u64 v[204:205], s[46:47], 0, v[172:173]
	s_mov_b32 m0, s67
	s_nop 0
	global_load_lds_dwordx4 v[204:205], off
	v_lshl_add_u64 v[204:205], s[46:47], 0, v[176:177]
	s_mov_b32 m0, s68
	s_nop 0
	global_load_lds_dwordx4 v[204:205], off
	s_waitcnt vmcnt(8)
	s_waitcnt lgkmcnt(0)
	s_barrier
	s_setprio 1
	s_waitcnt lgkmcnt(0)
	v_mfma_f32_16x16x32_bf16 v[60:63], v[72:75], v[160:163], v[60:63]
	v_mfma_f32_16x16x32_bf16 v[56:59], v[84:87], v[160:163], v[56:59]
	v_mfma_f32_16x16x32_bf16 v[44:47], v[72:75], v[168:171], v[44:47]
	v_mfma_f32_16x16x32_bf16 v[40:43], v[84:87], v[168:171], v[40:43]
	v_mfma_f32_16x16x32_bf16 v[28:31], v[72:75], v[188:191], v[28:31]
	v_mfma_f32_16x16x32_bf16 v[24:27], v[84:87], v[188:191], v[24:27]
	v_mfma_f32_16x16x32_bf16 v[12:15], v[72:75], v[196:199], v[12:15]
	v_mfma_f32_16x16x32_bf16 v[8:11], v[84:87], v[196:199], v[8:11]
	v_mfma_f32_16x16x32_bf16 v[60:63], v[76:79], v[164:167], v[60:63]
	v_mfma_f32_16x16x32_bf16 v[56:59], v[92:95], v[164:167], v[56:59]
	v_mfma_f32_16x16x32_bf16 v[44:47], v[76:79], v[184:187], v[44:47]
	v_mfma_f32_16x16x32_bf16 v[40:43], v[92:95], v[184:187], v[40:43]
	v_mfma_f32_16x16x32_bf16 v[28:31], v[76:79], v[192:195], v[28:31]
	v_mfma_f32_16x16x32_bf16 v[24:27], v[92:95], v[192:195], v[24:27]
	v_mfma_f32_16x16x32_bf16 v[12:15], v[76:79], v[200:203], v[12:15]
	v_mfma_f32_16x16x32_bf16 v[8:11], v[92:95], v[200:203], v[8:11]
	s_setprio 0
	s_setprio 1
	v_mfma_f32_16x16x32_bf16 v[52:55], v[144:147], v[160:163], v[52:55]
	v_mfma_f32_16x16x32_bf16 v[48:51], v[152:155], v[160:163], v[48:51]
	v_mfma_f32_16x16x32_bf16 v[36:39], v[144:147], v[168:171], v[36:39]
	v_mfma_f32_16x16x32_bf16 v[32:35], v[152:155], v[168:171], v[32:35]
	v_mfma_f32_16x16x32_bf16 v[20:23], v[144:147], v[188:191], v[20:23]
	v_mfma_f32_16x16x32_bf16 v[16:19], v[152:155], v[188:191], v[16:19]
	v_mfma_f32_16x16x32_bf16 v[4:7], v[144:147], v[196:199], v[4:7]
	v_mfma_f32_16x16x32_bf16 v[0:3], v[152:155], v[196:199], v[0:3]
	v_mfma_f32_16x16x32_bf16 v[52:55], v[148:151], v[164:167], v[52:55]
	v_mfma_f32_16x16x32_bf16 v[48:51], v[156:159], v[164:167], v[48:51]
	v_mfma_f32_16x16x32_bf16 v[36:39], v[148:151], v[184:187], v[36:39]
	v_mfma_f32_16x16x32_bf16 v[32:35], v[156:159], v[184:187], v[32:35]
	v_mfma_f32_16x16x32_bf16 v[20:23], v[148:151], v[192:195], v[20:23]
	v_mfma_f32_16x16x32_bf16 v[16:19], v[156:159], v[192:195], v[16:19]
	v_mfma_f32_16x16x32_bf16 v[4:7], v[148:151], v[200:203], v[4:7]
	v_mfma_f32_16x16x32_bf16 v[0:3], v[156:159], v[200:203], v[0:3]
	s_setprio 0
	v_add_u32_e32 v92, s30, v206
	v_add_u32_e32 v156, s52, v206
	s_add_i32 s76, s76, 2
	s_add_u32 s74, s74, 0x10000
	s_addc_u32 s75, s75, 0
	s_mov_b64 s[0:1], s[44:45]
	s_cmpk_gt_u32 s76, 0x7d
	s_barrier
	s_cbranch_scc0 .LBB0_1248
	s_and_b64 vcc, exec, s[22:23]
	s_cbranch_vccz .LBB0_1251
	s_barrier
